# router tails: logit quad sums and softmax max/sum shuffles as DPP / permlane-swap steps (18 serial ds_bpermute round trips per pass removed)
# speedup vs baseline: 1.0099x; 1.0099x over previous
; #define LAS __attribute__((address_space(3)))
; __device__ __forceinline__ void phase_norm2(const Params& p, const Ctx& F, const int l) {
;     ...
;         f32x2 lg[16];
;         unsigned wro = (unsigned)(uintptr_t)wr; asm volatile("" : "+v"(wro));
;         const LAS float* wr2 = (const LAS float*)(uintptr_t)wro;
; #pragma unroll
;         for (int e = 0; e < 16; ++e) { f32x2 a = {0.f, 0.f};
; #pragma unroll
;             for (int j = 0; j < 8; ++j) { const f32x4 w = *((const LAS f32x4*)(wr2 + e * DM) + F.lane + 64 * j);
; #pragma unroll
;                 for (int c = 0; c < 4; ++c) a += vv[j][c] * w[c]; }
;             lg[e] = a; }
.LBB0_937:
	s_or_b64 exec, exec, s[12:13]
	v_mov_b32_e32 v1, v35
	s_nop 0
	v_lshl_add_u32 v182, v132, 4, v1
	v_add_u32_e32 v244, 0x10000, v182
	ds_read_b128 v[224:227], v182
	ds_read_b128 v[228:231], v182 offset:1024
	ds_read_b128 v[232:235], v182 offset:2048
	ds_read_b128 v[236:239], v182 offset:3072
	s_waitcnt lgkmcnt(3)
	v_pk_fma_f32 v[156:157], v[124:125], v[224:225], 0 op_sel_hi:[1,0,0]
	s_nop 0
	v_pk_fma_f32 v[152:153], v[126:127], v[224:225], v[156:157] op_sel:[0,1,0]
	s_nop 0
	v_pk_fma_f32 v[152:153], v[128:129], v[226:227], v[152:153] op_sel_hi:[1,0,1]
	v_mov_b32_e32 v154, v227
	v_pk_fma_f32 v[156:157], v[130:131], v[154:155], v[152:153] op_sel_hi:[1,0,1]
	ds_read_b128 v[240:243], v182 offset:4096
	s_waitcnt lgkmcnt(3)
	v_pk_fma_f32 v[156:157], v[112:113], v[228:229], v[156:157] op_sel_hi:[1,0,1]
	s_nop 0
	v_pk_fma_f32 v[152:153], v[114:115], v[228:229], v[156:157] op_sel:[0,1,0]
	s_nop 0
	v_pk_fma_f32 v[152:153], v[118:119], v[230:231], v[152:153] op_sel_hi:[1,0,1]
	v_mov_b32_e32 v154, v231
	v_pk_fma_f32 v[156:157], v[122:123], v[154:155], v[152:153] op_sel_hi:[1,0,1]
	ds_read_b128 v[224:227], v182 offset:5120
	s_waitcnt lgkmcnt(3)
	v_pk_fma_f32 v[156:157], v[108:109], v[232:233], v[156:157] op_sel_hi:[1,0,1]
	s_nop 0
	v_pk_fma_f32 v[152:153], v[110:111], v[232:233], v[156:157] op_sel:[0,1,0]
	s_nop 0
	v_pk_fma_f32 v[152:153], v[116:117], v[234:235], v[152:153] op_sel_hi:[1,0,1]
	v_mov_b32_e32 v154, v235
	v_pk_fma_f32 v[156:157], v[120:121], v[154:155], v[152:153] op_sel_hi:[1,0,1]
	ds_read_b128 v[228:231], v182 offset:6144
	s_waitcnt lgkmcnt(3)
	v_pk_fma_f32 v[156:157], v[96:97], v[236:237], v[156:157] op_sel_hi:[1,0,1]
	s_nop 0
	v_pk_fma_f32 v[152:153], v[98:99], v[236:237], v[156:157] op_sel:[0,1,0]
	s_nop 0
	v_pk_fma_f32 v[152:153], v[102:103], v[238:239], v[152:153] op_sel_hi:[1,0,1]
	v_mov_b32_e32 v154, v239
	v_pk_fma_f32 v[156:157], v[106:107], v[154:155], v[152:153] op_sel_hi:[1,0,1]
	ds_read_b128 v[232:235], v182 offset:7168
	s_waitcnt lgkmcnt(3)
	v_pk_fma_f32 v[156:157], v[92:93], v[240:241], v[156:157] op_sel_hi:[1,0,1]
	s_nop 0
	v_pk_fma_f32 v[152:153], v[94:95], v[240:241], v[156:157] op_sel:[0,1,0]
	s_nop 0
	v_pk_fma_f32 v[152:153], v[100:101], v[242:243], v[152:153] op_sel_hi:[1,0,1]
	v_mov_b32_e32 v154, v243
	v_pk_fma_f32 v[156:157], v[104:105], v[154:155], v[152:153] op_sel_hi:[1,0,1]
	ds_read_b128 v[236:239], v182 offset:8192
	s_waitcnt lgkmcnt(3)
	v_pk_fma_f32 v[156:157], v[80:81], v[224:225], v[156:157] op_sel_hi:[1,0,1]
	s_nop 0
	v_pk_fma_f32 v[152:153], v[82:83], v[224:225], v[156:157] op_sel:[0,1,0]
	s_nop 0
	v_pk_fma_f32 v[152:153], v[86:87], v[226:227], v[152:153] op_sel_hi:[1,0,1]
	v_mov_b32_e32 v154, v227
	v_pk_fma_f32 v[156:157], v[90:91], v[154:155], v[152:153] op_sel_hi:[1,0,1]
	ds_read_b128 v[240:243], v182 offset:9216
	s_waitcnt lgkmcnt(3)
	v_pk_fma_f32 v[156:157], v[76:77], v[228:229], v[156:157] op_sel_hi:[1,0,1]
	s_nop 0
	v_pk_fma_f32 v[152:153], v[78:79], v[228:229], v[156:157] op_sel:[0,1,0]
	s_nop 0
	v_pk_fma_f32 v[152:153], v[84:85], v[230:231], v[152:153] op_sel_hi:[1,0,1]
	v_mov_b32_e32 v154, v231
	v_pk_fma_f32 v[156:157], v[88:89], v[154:155], v[152:153] op_sel_hi:[1,0,1]
	ds_read_b128 v[224:227], v182 offset:10240
	s_waitcnt lgkmcnt(3)
	v_pk_fma_f32 v[156:157], v[68:69], v[232:233], v[156:157] op_sel_hi:[1,0,1]
	s_nop 0
	v_pk_fma_f32 v[152:153], v[70:71], v[232:233], v[156:157] op_sel:[0,1,0]
	s_nop 0
	v_pk_fma_f32 v[152:153], v[72:73], v[234:235], v[152:153] op_sel_hi:[1,0,1]
	v_mov_b32_e32 v154, v235
	v_pk_fma_f32 v[152:153], v[74:75], v[154:155], v[152:153] op_sel_hi:[1,0,1]
	ds_read_b128 v[228:231], v182 offset:11264
	s_waitcnt lgkmcnt(3)
	v_pk_fma_f32 v[158:159], v[124:125], v[236:237], 0 op_sel_hi:[1,0,0]
	s_nop 0
	v_pk_fma_f32 v[154:155], v[126:127], v[236:237], v[158:159] op_sel:[0,1,0]
	s_nop 0
	v_pk_fma_f32 v[154:155], v[128:129], v[238:239], v[154:155] op_sel_hi:[1,0,1]
	v_mov_b32_e32 v156, v239
	v_pk_fma_f32 v[158:159], v[130:131], v[156:157], v[154:155] op_sel_hi:[1,0,1]
	ds_read_b128 v[232:235], v182 offset:12288
	s_waitcnt lgkmcnt(3)
	v_pk_fma_f32 v[158:159], v[112:113], v[240:241], v[158:159] op_sel_hi:[1,0,1]
	s_nop 0
	v_pk_fma_f32 v[154:155], v[114:115], v[240:241], v[158:159] op_sel:[0,1,0]
	s_nop 0
	v_pk_fma_f32 v[154:155], v[118:119], v[242:243], v[154:155] op_sel_hi:[1,0,1]
	v_mov_b32_e32 v156, v243
	v_pk_fma_f32 v[158:159], v[122:123], v[156:157], v[154:155] op_sel_hi:[1,0,1]
	ds_read_b128 v[236:239], v182 offset:13312
	s_waitcnt lgkmcnt(3)
	v_pk_fma_f32 v[158:159], v[108:109], v[224:225], v[158:159] op_sel_hi:[1,0,1]
	s_nop 0
	v_pk_fma_f32 v[154:155], v[110:111], v[224:225], v[158:159] op_sel:[0,1,0]
	s_nop 0
	v_pk_fma_f32 v[154:155], v[116:117], v[226:227], v[154:155] op_sel_hi:[1,0,1]
	v_mov_b32_e32 v156, v227
	v_pk_fma_f32 v[158:159], v[120:121], v[156:157], v[154:155] op_sel_hi:[1,0,1]
	ds_read_b128 v[240:243], v182 offset:14336
	s_waitcnt lgkmcnt(3)
	v_pk_fma_f32 v[158:159], v[96:97], v[228:229], v[158:159] op_sel_hi:[1,0,1]
	s_nop 0
	v_pk_fma_f32 v[154:155], v[98:99], v[228:229], v[158:159] op_sel:[0,1,0]
	s_nop 0
	v_pk_fma_f32 v[154:155], v[102:103], v[230:231], v[154:155] op_sel_hi:[1,0,1]
	v_mov_b32_e32 v156, v231
	v_pk_fma_f32 v[158:159], v[106:107], v[156:157], v[154:155] op_sel_hi:[1,0,1]
	ds_read_b128 v[224:227], v182 offset:15360
	s_waitcnt lgkmcnt(3)
	v_pk_fma_f32 v[158:159], v[92:93], v[232:233], v[158:159] op_sel_hi:[1,0,1]
	s_nop 0
	v_pk_fma_f32 v[154:155], v[94:95], v[232:233], v[158:159] op_sel:[0,1,0]
	s_nop 0
	v_pk_fma_f32 v[154:155], v[100:101], v[234:235], v[154:155] op_sel_hi:[1,0,1]
	v_mov_b32_e32 v156, v235
	v_pk_fma_f32 v[158:159], v[104:105], v[156:157], v[154:155] op_sel_hi:[1,0,1]
	ds_read_b128 v[228:231], v182 offset:16384
	s_waitcnt lgkmcnt(3)
; #define LAS __attribute__((address_space(3)))
; __device__ __forceinline__ void phase_norm2(const Params& p, const Ctx& F, const int l) {
;     ...
;         f32x2 lg[16];
;         unsigned wro = (unsigned)(uintptr_t)wr; asm volatile("" : "+v"(wro));
;         const LAS float* wr2 = (const LAS float*)(uintptr_t)wro;
; #pragma unroll
;         for (int e = 0; e < 16; ++e) { f32x2 a = {0.f, 0.f};
; #pragma unroll
;             for (int j = 0; j < 8; ++j) { const f32x4 w = *((const LAS f32x4*)(wr2 + e * DM) + F.lane + 64 * j);
; #pragma unroll
;                 for (int c = 0; c < 4; ++c) a += vv[j][c] * w[c]; }
;             lg[e] = a; }
	v_pk_fma_f32 v[158:159], v[80:81], v[236:237], v[158:159] op_sel_hi:[1,0,1]
	s_nop 0
	v_pk_fma_f32 v[154:155], v[82:83], v[236:237], v[158:159] op_sel:[0,1,0]
	s_nop 0
	v_pk_fma_f32 v[154:155], v[86:87], v[238:239], v[154:155] op_sel_hi:[1,0,1]
	v_mov_b32_e32 v156, v239
	v_pk_fma_f32 v[158:159], v[90:91], v[156:157], v[154:155] op_sel_hi:[1,0,1]
	ds_read_b128 v[232:235], v182 offset:17408
	s_waitcnt lgkmcnt(3)
	v_pk_fma_f32 v[158:159], v[76:77], v[240:241], v[158:159] op_sel_hi:[1,0,1]
	s_nop 0
	v_pk_fma_f32 v[154:155], v[78:79], v[240:241], v[158:159] op_sel:[0,1,0]
	s_nop 0
	v_pk_fma_f32 v[154:155], v[84:85], v[242:243], v[154:155] op_sel_hi:[1,0,1]
	v_mov_b32_e32 v156, v243
	v_pk_fma_f32 v[158:159], v[88:89], v[156:157], v[154:155] op_sel_hi:[1,0,1]
	ds_read_b128 v[236:239], v182 offset:18432
	s_waitcnt lgkmcnt(3)
	v_pk_fma_f32 v[158:159], v[68:69], v[224:225], v[158:159] op_sel_hi:[1,0,1]
	s_nop 0
	v_pk_fma_f32 v[154:155], v[70:71], v[224:225], v[158:159] op_sel:[0,1,0]
	s_nop 0
	v_pk_fma_f32 v[154:155], v[72:73], v[226:227], v[154:155] op_sel_hi:[1,0,1]
	v_mov_b32_e32 v156, v227
	v_pk_fma_f32 v[154:155], v[74:75], v[156:157], v[154:155] op_sel_hi:[1,0,1]
	ds_read_b128 v[240:243], v182 offset:19456
	s_waitcnt lgkmcnt(3)
	v_pk_fma_f32 v[160:161], v[124:125], v[228:229], 0 op_sel_hi:[1,0,0]
	s_nop 0
	v_pk_fma_f32 v[156:157], v[126:127], v[228:229], v[160:161] op_sel:[0,1,0]
	s_nop 0
	v_pk_fma_f32 v[156:157], v[128:129], v[230:231], v[156:157] op_sel_hi:[1,0,1]
	v_mov_b32_e32 v158, v231
	v_pk_fma_f32 v[160:161], v[130:131], v[158:159], v[156:157] op_sel_hi:[1,0,1]
	ds_read_b128 v[224:227], v182 offset:20480
	s_waitcnt lgkmcnt(3)
	v_pk_fma_f32 v[160:161], v[112:113], v[232:233], v[160:161] op_sel_hi:[1,0,1]
	s_nop 0
	v_pk_fma_f32 v[156:157], v[114:115], v[232:233], v[160:161] op_sel:[0,1,0]
	s_nop 0
	v_pk_fma_f32 v[156:157], v[118:119], v[234:235], v[156:157] op_sel_hi:[1,0,1]
	v_mov_b32_e32 v158, v235
	v_pk_fma_f32 v[160:161], v[122:123], v[158:159], v[156:157] op_sel_hi:[1,0,1]
	ds_read_b128 v[228:231], v182 offset:21504
	s_waitcnt lgkmcnt(3)
	v_pk_fma_f32 v[160:161], v[108:109], v[236:237], v[160:161] op_sel_hi:[1,0,1]
	s_nop 0
	v_pk_fma_f32 v[156:157], v[110:111], v[236:237], v[160:161] op_sel:[0,1,0]
	s_nop 0
	v_pk_fma_f32 v[156:157], v[116:117], v[238:239], v[156:157] op_sel_hi:[1,0,1]
	v_mov_b32_e32 v158, v239
	v_pk_fma_f32 v[160:161], v[120:121], v[158:159], v[156:157] op_sel_hi:[1,0,1]
	ds_read_b128 v[232:235], v182 offset:22528
	s_waitcnt lgkmcnt(3)
	v_pk_fma_f32 v[160:161], v[96:97], v[240:241], v[160:161] op_sel_hi:[1,0,1]
	s_nop 0
	v_pk_fma_f32 v[156:157], v[98:99], v[240:241], v[160:161] op_sel:[0,1,0]
	s_nop 0
	v_pk_fma_f32 v[156:157], v[102:103], v[242:243], v[156:157] op_sel_hi:[1,0,1]
	v_mov_b32_e32 v158, v243
	v_pk_fma_f32 v[160:161], v[106:107], v[158:159], v[156:157] op_sel_hi:[1,0,1]
	ds_read_b128 v[236:239], v182 offset:23552
	s_waitcnt lgkmcnt(3)
	v_pk_fma_f32 v[160:161], v[92:93], v[224:225], v[160:161] op_sel_hi:[1,0,1]
	s_nop 0
	v_pk_fma_f32 v[156:157], v[94:95], v[224:225], v[160:161] op_sel:[0,1,0]
	s_nop 0
	v_pk_fma_f32 v[156:157], v[100:101], v[226:227], v[156:157] op_sel_hi:[1,0,1]
	v_mov_b32_e32 v158, v227
	v_pk_fma_f32 v[160:161], v[104:105], v[158:159], v[156:157] op_sel_hi:[1,0,1]
	ds_read_b128 v[240:243], v182 offset:24576
	s_waitcnt lgkmcnt(3)
	v_pk_fma_f32 v[160:161], v[80:81], v[228:229], v[160:161] op_sel_hi:[1,0,1]
	s_nop 0
	v_pk_fma_f32 v[156:157], v[82:83], v[228:229], v[160:161] op_sel:[0,1,0]
	s_nop 0
	v_pk_fma_f32 v[156:157], v[86:87], v[230:231], v[156:157] op_sel_hi:[1,0,1]
	v_mov_b32_e32 v158, v231
	v_pk_fma_f32 v[160:161], v[90:91], v[158:159], v[156:157] op_sel_hi:[1,0,1]
	ds_read_b128 v[224:227], v182 offset:25600
	s_waitcnt lgkmcnt(3)
	v_pk_fma_f32 v[160:161], v[76:77], v[232:233], v[160:161] op_sel_hi:[1,0,1]
	s_nop 0
	v_pk_fma_f32 v[156:157], v[78:79], v[232:233], v[160:161] op_sel:[0,1,0]
	s_nop 0
	v_pk_fma_f32 v[156:157], v[84:85], v[234:235], v[156:157] op_sel_hi:[1,0,1]
	v_mov_b32_e32 v158, v235
	v_pk_fma_f32 v[160:161], v[88:89], v[158:159], v[156:157] op_sel_hi:[1,0,1]
	ds_read_b128 v[228:231], v182 offset:26624
	s_waitcnt lgkmcnt(3)
	v_pk_fma_f32 v[160:161], v[68:69], v[236:237], v[160:161] op_sel_hi:[1,0,1]
	s_nop 0
	v_pk_fma_f32 v[156:157], v[70:71], v[236:237], v[160:161] op_sel:[0,1,0]
	s_nop 0
	v_pk_fma_f32 v[156:157], v[72:73], v[238:239], v[156:157] op_sel_hi:[1,0,1]
	v_mov_b32_e32 v158, v239
	v_pk_fma_f32 v[156:157], v[74:75], v[158:159], v[156:157] op_sel_hi:[1,0,1]
	ds_read_b128 v[232:235], v182 offset:27648
	s_waitcnt lgkmcnt(3)
	v_pk_fma_f32 v[162:163], v[124:125], v[240:241], 0 op_sel_hi:[1,0,0]
	s_nop 0
	v_pk_fma_f32 v[158:159], v[126:127], v[240:241], v[162:163] op_sel:[0,1,0]
	s_nop 0
	v_pk_fma_f32 v[158:159], v[128:129], v[242:243], v[158:159] op_sel_hi:[1,0,1]
	v_mov_b32_e32 v160, v243
	v_pk_fma_f32 v[162:163], v[130:131], v[160:161], v[158:159] op_sel_hi:[1,0,1]
	ds_read_b128 v[236:239], v182 offset:28672
	s_waitcnt lgkmcnt(3)
	v_pk_fma_f32 v[162:163], v[112:113], v[224:225], v[162:163] op_sel_hi:[1,0,1]
	s_nop 0
	v_pk_fma_f32 v[158:159], v[114:115], v[224:225], v[162:163] op_sel:[0,1,0]
	s_nop 0
	v_pk_fma_f32 v[158:159], v[118:119], v[226:227], v[158:159] op_sel_hi:[1,0,1]
	v_mov_b32_e32 v160, v227
	v_pk_fma_f32 v[162:163], v[122:123], v[160:161], v[158:159] op_sel_hi:[1,0,1]
	ds_read_b128 v[240:243], v182 offset:29696
	s_waitcnt lgkmcnt(3)
	v_pk_fma_f32 v[162:163], v[108:109], v[228:229], v[162:163] op_sel_hi:[1,0,1]
	s_nop 0
	v_pk_fma_f32 v[158:159], v[110:111], v[228:229], v[162:163] op_sel:[0,1,0]
	s_nop 0
	v_pk_fma_f32 v[158:159], v[116:117], v[230:231], v[158:159] op_sel_hi:[1,0,1]
	v_mov_b32_e32 v160, v231
	v_pk_fma_f32 v[162:163], v[120:121], v[160:161], v[158:159] op_sel_hi:[1,0,1]
	ds_read_b128 v[224:227], v182 offset:30720
	s_waitcnt lgkmcnt(3)
; #define LAS __attribute__((address_space(3)))
; __device__ __forceinline__ void phase_norm2(const Params& p, const Ctx& F, const int l) {
;     ...
;         f32x2 lg[16];
;         unsigned wro = (unsigned)(uintptr_t)wr; asm volatile("" : "+v"(wro));
;         const LAS float* wr2 = (const LAS float*)(uintptr_t)wro;
; #pragma unroll
;         for (int e = 0; e < 16; ++e) { f32x2 a = {0.f, 0.f};
; #pragma unroll
;             for (int j = 0; j < 8; ++j) { const f32x4 w = *((const LAS f32x4*)(wr2 + e * DM) + F.lane + 64 * j);
; #pragma unroll
;                 for (int c = 0; c < 4; ++c) a += vv[j][c] * w[c]; }
;             lg[e] = a; }
	v_pk_fma_f32 v[162:163], v[96:97], v[232:233], v[162:163] op_sel_hi:[1,0,1]
	s_nop 0
	v_pk_fma_f32 v[158:159], v[98:99], v[232:233], v[162:163] op_sel:[0,1,0]
	s_nop 0
	v_pk_fma_f32 v[158:159], v[102:103], v[234:235], v[158:159] op_sel_hi:[1,0,1]
	v_mov_b32_e32 v160, v235
	v_pk_fma_f32 v[162:163], v[106:107], v[160:161], v[158:159] op_sel_hi:[1,0,1]
	ds_read_b128 v[228:231], v182 offset:31744
	s_waitcnt lgkmcnt(3)
	v_pk_fma_f32 v[162:163], v[92:93], v[236:237], v[162:163] op_sel_hi:[1,0,1]
	s_nop 0
	v_pk_fma_f32 v[158:159], v[94:95], v[236:237], v[162:163] op_sel:[0,1,0]
	s_nop 0
	v_pk_fma_f32 v[158:159], v[100:101], v[238:239], v[158:159] op_sel_hi:[1,0,1]
	v_mov_b32_e32 v160, v239
	v_pk_fma_f32 v[162:163], v[104:105], v[160:161], v[158:159] op_sel_hi:[1,0,1]
	ds_read_b128 v[232:235], v182 offset:32768
	s_waitcnt lgkmcnt(3)
	v_pk_fma_f32 v[162:163], v[80:81], v[240:241], v[162:163] op_sel_hi:[1,0,1]
	s_nop 0
	v_pk_fma_f32 v[158:159], v[82:83], v[240:241], v[162:163] op_sel:[0,1,0]
	s_nop 0
	v_pk_fma_f32 v[158:159], v[86:87], v[242:243], v[158:159] op_sel_hi:[1,0,1]
	v_mov_b32_e32 v160, v243
	v_pk_fma_f32 v[162:163], v[90:91], v[160:161], v[158:159] op_sel_hi:[1,0,1]
	ds_read_b128 v[236:239], v182 offset:33792
	s_waitcnt lgkmcnt(3)
	v_pk_fma_f32 v[162:163], v[76:77], v[224:225], v[162:163] op_sel_hi:[1,0,1]
	s_nop 0
	v_pk_fma_f32 v[158:159], v[78:79], v[224:225], v[162:163] op_sel:[0,1,0]
	s_nop 0
	v_pk_fma_f32 v[158:159], v[84:85], v[226:227], v[158:159] op_sel_hi:[1,0,1]
	v_mov_b32_e32 v160, v227
	v_pk_fma_f32 v[162:163], v[88:89], v[160:161], v[158:159] op_sel_hi:[1,0,1]
	ds_read_b128 v[240:243], v182 offset:34816
	s_waitcnt lgkmcnt(3)
	v_pk_fma_f32 v[162:163], v[68:69], v[228:229], v[162:163] op_sel_hi:[1,0,1]
	s_nop 0
	v_pk_fma_f32 v[158:159], v[70:71], v[228:229], v[162:163] op_sel:[0,1,0]
	s_nop 0
	v_pk_fma_f32 v[158:159], v[72:73], v[230:231], v[158:159] op_sel_hi:[1,0,1]
	v_mov_b32_e32 v160, v231
	v_pk_fma_f32 v[158:159], v[74:75], v[160:161], v[158:159] op_sel_hi:[1,0,1]
	ds_read_b128 v[224:227], v182 offset:35840
	s_waitcnt lgkmcnt(3)
	v_pk_fma_f32 v[164:165], v[124:125], v[232:233], 0 op_sel_hi:[1,0,0]
	s_nop 0
	v_pk_fma_f32 v[160:161], v[126:127], v[232:233], v[164:165] op_sel:[0,1,0]
	s_nop 0
	v_pk_fma_f32 v[160:161], v[128:129], v[234:235], v[160:161] op_sel_hi:[1,0,1]
	v_mov_b32_e32 v162, v235
	v_pk_fma_f32 v[164:165], v[130:131], v[162:163], v[160:161] op_sel_hi:[1,0,1]
	ds_read_b128 v[228:231], v182 offset:36864
	s_waitcnt lgkmcnt(3)
	v_pk_fma_f32 v[164:165], v[112:113], v[236:237], v[164:165] op_sel_hi:[1,0,1]
	s_nop 0
	v_pk_fma_f32 v[160:161], v[114:115], v[236:237], v[164:165] op_sel:[0,1,0]
	s_nop 0
	v_pk_fma_f32 v[160:161], v[118:119], v[238:239], v[160:161] op_sel_hi:[1,0,1]
	v_mov_b32_e32 v162, v239
	v_pk_fma_f32 v[164:165], v[122:123], v[162:163], v[160:161] op_sel_hi:[1,0,1]
	ds_read_b128 v[232:235], v182 offset:37888
	s_waitcnt lgkmcnt(3)
	v_pk_fma_f32 v[164:165], v[108:109], v[240:241], v[164:165] op_sel_hi:[1,0,1]
	s_nop 0
	v_pk_fma_f32 v[160:161], v[110:111], v[240:241], v[164:165] op_sel:[0,1,0]
	s_nop 0
	v_pk_fma_f32 v[160:161], v[116:117], v[242:243], v[160:161] op_sel_hi:[1,0,1]
	v_mov_b32_e32 v162, v243
	v_pk_fma_f32 v[164:165], v[120:121], v[162:163], v[160:161] op_sel_hi:[1,0,1]
	ds_read_b128 v[236:239], v182 offset:38912
	s_waitcnt lgkmcnt(3)
	v_pk_fma_f32 v[164:165], v[96:97], v[224:225], v[164:165] op_sel_hi:[1,0,1]
	s_nop 0
	v_pk_fma_f32 v[160:161], v[98:99], v[224:225], v[164:165] op_sel:[0,1,0]
	s_nop 0
	v_pk_fma_f32 v[160:161], v[102:103], v[226:227], v[160:161] op_sel_hi:[1,0,1]
	v_mov_b32_e32 v162, v227
	v_pk_fma_f32 v[164:165], v[106:107], v[162:163], v[160:161] op_sel_hi:[1,0,1]
	ds_read_b128 v[240:243], v182 offset:39936
	s_waitcnt lgkmcnt(3)
	v_pk_fma_f32 v[164:165], v[92:93], v[228:229], v[164:165] op_sel_hi:[1,0,1]
	s_nop 0
	v_pk_fma_f32 v[160:161], v[94:95], v[228:229], v[164:165] op_sel:[0,1,0]
	s_nop 0
	v_pk_fma_f32 v[160:161], v[100:101], v[230:231], v[160:161] op_sel_hi:[1,0,1]
	v_mov_b32_e32 v162, v231
	v_pk_fma_f32 v[164:165], v[104:105], v[162:163], v[160:161] op_sel_hi:[1,0,1]
	ds_read_b128 v[224:227], v182 offset:40960
	s_waitcnt lgkmcnt(3)
	v_pk_fma_f32 v[164:165], v[80:81], v[232:233], v[164:165] op_sel_hi:[1,0,1]
	s_nop 0
	v_pk_fma_f32 v[160:161], v[82:83], v[232:233], v[164:165] op_sel:[0,1,0]
	s_nop 0
	v_pk_fma_f32 v[160:161], v[86:87], v[234:235], v[160:161] op_sel_hi:[1,0,1]
	v_mov_b32_e32 v162, v235
	v_pk_fma_f32 v[164:165], v[90:91], v[162:163], v[160:161] op_sel_hi:[1,0,1]
	ds_read_b128 v[228:231], v182 offset:41984
	s_waitcnt lgkmcnt(3)
	v_pk_fma_f32 v[164:165], v[76:77], v[236:237], v[164:165] op_sel_hi:[1,0,1]
	s_nop 0
	v_pk_fma_f32 v[160:161], v[78:79], v[236:237], v[164:165] op_sel:[0,1,0]
	s_nop 0
	v_pk_fma_f32 v[160:161], v[84:85], v[238:239], v[160:161] op_sel_hi:[1,0,1]
	v_mov_b32_e32 v162, v239
	v_pk_fma_f32 v[164:165], v[88:89], v[162:163], v[160:161] op_sel_hi:[1,0,1]
	ds_read_b128 v[232:235], v182 offset:43008
	s_waitcnt lgkmcnt(3)
	v_pk_fma_f32 v[164:165], v[68:69], v[240:241], v[164:165] op_sel_hi:[1,0,1]
	s_nop 0
	v_pk_fma_f32 v[160:161], v[70:71], v[240:241], v[164:165] op_sel:[0,1,0]
	s_nop 0
	v_pk_fma_f32 v[160:161], v[72:73], v[242:243], v[160:161] op_sel_hi:[1,0,1]
	v_mov_b32_e32 v162, v243
	v_pk_fma_f32 v[160:161], v[74:75], v[162:163], v[160:161] op_sel_hi:[1,0,1]
	ds_read_b128 v[236:239], v182 offset:44032
	s_waitcnt lgkmcnt(3)
	v_pk_fma_f32 v[166:167], v[124:125], v[224:225], 0 op_sel_hi:[1,0,0]
	s_nop 0
	v_pk_fma_f32 v[162:163], v[126:127], v[224:225], v[166:167] op_sel:[0,1,0]
	s_nop 0
	v_pk_fma_f32 v[162:163], v[128:129], v[226:227], v[162:163] op_sel_hi:[1,0,1]
	v_mov_b32_e32 v164, v227
	v_pk_fma_f32 v[166:167], v[130:131], v[164:165], v[162:163] op_sel_hi:[1,0,1]
	ds_read_b128 v[240:243], v182 offset:45056
	s_waitcnt lgkmcnt(3)
; #define LAS __attribute__((address_space(3)))
; __device__ __forceinline__ void phase_norm2(const Params& p, const Ctx& F, const int l) {
;     ...
;         f32x2 lg[16];
;         unsigned wro = (unsigned)(uintptr_t)wr; asm volatile("" : "+v"(wro));
;         const LAS float* wr2 = (const LAS float*)(uintptr_t)wro;
; #pragma unroll
;         for (int e = 0; e < 16; ++e) { f32x2 a = {0.f, 0.f};
; #pragma unroll
;             for (int j = 0; j < 8; ++j) { const f32x4 w = *((const LAS f32x4*)(wr2 + e * DM) + F.lane + 64 * j);
; #pragma unroll
;                 for (int c = 0; c < 4; ++c) a += vv[j][c] * w[c]; }
;             lg[e] = a; }
	v_pk_fma_f32 v[166:167], v[112:113], v[228:229], v[166:167] op_sel_hi:[1,0,1]
	s_nop 0
	v_pk_fma_f32 v[162:163], v[114:115], v[228:229], v[166:167] op_sel:[0,1,0]
	s_nop 0
	v_pk_fma_f32 v[162:163], v[118:119], v[230:231], v[162:163] op_sel_hi:[1,0,1]
	v_mov_b32_e32 v164, v231
	v_pk_fma_f32 v[166:167], v[122:123], v[164:165], v[162:163] op_sel_hi:[1,0,1]
	ds_read_b128 v[224:227], v182 offset:46080
	s_waitcnt lgkmcnt(3)
	v_pk_fma_f32 v[166:167], v[108:109], v[232:233], v[166:167] op_sel_hi:[1,0,1]
	s_nop 0
	v_pk_fma_f32 v[162:163], v[110:111], v[232:233], v[166:167] op_sel:[0,1,0]
	s_nop 0
	v_pk_fma_f32 v[162:163], v[116:117], v[234:235], v[162:163] op_sel_hi:[1,0,1]
	v_mov_b32_e32 v164, v235
	v_pk_fma_f32 v[166:167], v[120:121], v[164:165], v[162:163] op_sel_hi:[1,0,1]
	ds_read_b128 v[228:231], v182 offset:47104
	s_waitcnt lgkmcnt(3)
	v_pk_fma_f32 v[166:167], v[96:97], v[236:237], v[166:167] op_sel_hi:[1,0,1]
	s_nop 0
	v_pk_fma_f32 v[162:163], v[98:99], v[236:237], v[166:167] op_sel:[0,1,0]
	s_nop 0
	v_pk_fma_f32 v[162:163], v[102:103], v[238:239], v[162:163] op_sel_hi:[1,0,1]
	v_mov_b32_e32 v164, v239
	v_pk_fma_f32 v[166:167], v[106:107], v[164:165], v[162:163] op_sel_hi:[1,0,1]
	ds_read_b128 v[232:235], v182 offset:48128
	s_waitcnt lgkmcnt(3)
	v_pk_fma_f32 v[166:167], v[92:93], v[240:241], v[166:167] op_sel_hi:[1,0,1]
	s_nop 0
	v_pk_fma_f32 v[162:163], v[94:95], v[240:241], v[166:167] op_sel:[0,1,0]
	s_nop 0
	v_pk_fma_f32 v[162:163], v[100:101], v[242:243], v[162:163] op_sel_hi:[1,0,1]
	v_mov_b32_e32 v164, v243
	v_pk_fma_f32 v[166:167], v[104:105], v[164:165], v[162:163] op_sel_hi:[1,0,1]
	ds_read_b128 v[236:239], v182 offset:49152
	s_waitcnt lgkmcnt(3)
	v_pk_fma_f32 v[166:167], v[80:81], v[224:225], v[166:167] op_sel_hi:[1,0,1]
	s_nop 0
	v_pk_fma_f32 v[162:163], v[82:83], v[224:225], v[166:167] op_sel:[0,1,0]
	s_nop 0
	v_pk_fma_f32 v[162:163], v[86:87], v[226:227], v[162:163] op_sel_hi:[1,0,1]
	v_mov_b32_e32 v164, v227
	v_pk_fma_f32 v[166:167], v[90:91], v[164:165], v[162:163] op_sel_hi:[1,0,1]
	ds_read_b128 v[240:243], v182 offset:50176
	s_waitcnt lgkmcnt(3)
	v_pk_fma_f32 v[166:167], v[76:77], v[228:229], v[166:167] op_sel_hi:[1,0,1]
	s_nop 0
	v_pk_fma_f32 v[162:163], v[78:79], v[228:229], v[166:167] op_sel:[0,1,0]
	s_nop 0
	v_pk_fma_f32 v[162:163], v[84:85], v[230:231], v[162:163] op_sel_hi:[1,0,1]
	v_mov_b32_e32 v164, v231
	v_pk_fma_f32 v[166:167], v[88:89], v[164:165], v[162:163] op_sel_hi:[1,0,1]
	ds_read_b128 v[224:227], v182 offset:51200
	s_waitcnt lgkmcnt(3)
	v_pk_fma_f32 v[166:167], v[68:69], v[232:233], v[166:167] op_sel_hi:[1,0,1]
	s_nop 0
	v_pk_fma_f32 v[162:163], v[70:71], v[232:233], v[166:167] op_sel:[0,1,0]
	s_nop 0
	v_pk_fma_f32 v[162:163], v[72:73], v[234:235], v[162:163] op_sel_hi:[1,0,1]
	v_mov_b32_e32 v164, v235
	v_pk_fma_f32 v[162:163], v[74:75], v[164:165], v[162:163] op_sel_hi:[1,0,1]
	ds_read_b128 v[228:231], v182 offset:52224
	s_waitcnt lgkmcnt(3)
	v_pk_fma_f32 v[168:169], v[124:125], v[236:237], 0 op_sel_hi:[1,0,0]
	s_nop 0
	v_pk_fma_f32 v[164:165], v[126:127], v[236:237], v[168:169] op_sel:[0,1,0]
	s_nop 0
	v_pk_fma_f32 v[164:165], v[128:129], v[238:239], v[164:165] op_sel_hi:[1,0,1]
	v_mov_b32_e32 v166, v239
	v_pk_fma_f32 v[168:169], v[130:131], v[166:167], v[164:165] op_sel_hi:[1,0,1]
	ds_read_b128 v[232:235], v182 offset:53248
	s_waitcnt lgkmcnt(3)
	v_pk_fma_f32 v[168:169], v[112:113], v[240:241], v[168:169] op_sel_hi:[1,0,1]
	s_nop 0
	v_pk_fma_f32 v[164:165], v[114:115], v[240:241], v[168:169] op_sel:[0,1,0]
	s_nop 0
	v_pk_fma_f32 v[164:165], v[118:119], v[242:243], v[164:165] op_sel_hi:[1,0,1]
	v_mov_b32_e32 v166, v243
	v_pk_fma_f32 v[168:169], v[122:123], v[166:167], v[164:165] op_sel_hi:[1,0,1]
	ds_read_b128 v[236:239], v182 offset:54272
	s_waitcnt lgkmcnt(3)
	v_pk_fma_f32 v[168:169], v[108:109], v[224:225], v[168:169] op_sel_hi:[1,0,1]
	s_nop 0
	v_pk_fma_f32 v[164:165], v[110:111], v[224:225], v[168:169] op_sel:[0,1,0]
	s_nop 0
	v_pk_fma_f32 v[164:165], v[116:117], v[226:227], v[164:165] op_sel_hi:[1,0,1]
	v_mov_b32_e32 v166, v227
	v_pk_fma_f32 v[168:169], v[120:121], v[166:167], v[164:165] op_sel_hi:[1,0,1]
	ds_read_b128 v[240:243], v182 offset:55296
	s_waitcnt lgkmcnt(3)
	v_pk_fma_f32 v[168:169], v[96:97], v[228:229], v[168:169] op_sel_hi:[1,0,1]
	s_nop 0
	v_pk_fma_f32 v[164:165], v[98:99], v[228:229], v[168:169] op_sel:[0,1,0]
	s_nop 0
	v_pk_fma_f32 v[164:165], v[102:103], v[230:231], v[164:165] op_sel_hi:[1,0,1]
	v_mov_b32_e32 v166, v231
	v_pk_fma_f32 v[168:169], v[106:107], v[166:167], v[164:165] op_sel_hi:[1,0,1]
	ds_read_b128 v[224:227], v182 offset:56320
	s_waitcnt lgkmcnt(3)
	v_pk_fma_f32 v[168:169], v[92:93], v[232:233], v[168:169] op_sel_hi:[1,0,1]
	s_nop 0
	v_pk_fma_f32 v[164:165], v[94:95], v[232:233], v[168:169] op_sel:[0,1,0]
	s_nop 0
	v_pk_fma_f32 v[164:165], v[100:101], v[234:235], v[164:165] op_sel_hi:[1,0,1]
	v_mov_b32_e32 v166, v235
	v_pk_fma_f32 v[168:169], v[104:105], v[166:167], v[164:165] op_sel_hi:[1,0,1]
	ds_read_b128 v[228:231], v182 offset:57344
	s_waitcnt lgkmcnt(3)
	v_pk_fma_f32 v[168:169], v[80:81], v[236:237], v[168:169] op_sel_hi:[1,0,1]
	s_nop 0
	v_pk_fma_f32 v[164:165], v[82:83], v[236:237], v[168:169] op_sel:[0,1,0]
	s_nop 0
	v_pk_fma_f32 v[164:165], v[86:87], v[238:239], v[164:165] op_sel_hi:[1,0,1]
	v_mov_b32_e32 v166, v239
	v_pk_fma_f32 v[168:169], v[90:91], v[166:167], v[164:165] op_sel_hi:[1,0,1]
	ds_read_b128 v[232:235], v182 offset:58368
	s_waitcnt lgkmcnt(3)
; #define LAS __attribute__((address_space(3)))
; __device__ __forceinline__ void phase_norm2(const Params& p, const Ctx& F, const int l) {
;     ...
;         f32x2 lg[16];
;         unsigned wro = (unsigned)(uintptr_t)wr; asm volatile("" : "+v"(wro));
;         const LAS float* wr2 = (const LAS float*)(uintptr_t)wro;
; #pragma unroll
;         for (int e = 0; e < 16; ++e) { f32x2 a = {0.f, 0.f};
; #pragma unroll
;             for (int j = 0; j < 8; ++j) { const f32x4 w = *((const LAS f32x4*)(wr2 + e * DM) + F.lane + 64 * j);
; #pragma unroll
;                 for (int c = 0; c < 4; ++c) a += vv[j][c] * w[c]; }
;             lg[e] = a; }
	v_pk_fma_f32 v[168:169], v[76:77], v[240:241], v[168:169] op_sel_hi:[1,0,1]
	s_nop 0
	v_pk_fma_f32 v[164:165], v[78:79], v[240:241], v[168:169] op_sel:[0,1,0]
	s_nop 0
	v_pk_fma_f32 v[164:165], v[84:85], v[242:243], v[164:165] op_sel_hi:[1,0,1]
	v_mov_b32_e32 v166, v243
	v_pk_fma_f32 v[168:169], v[88:89], v[166:167], v[164:165] op_sel_hi:[1,0,1]
	ds_read_b128 v[236:239], v182 offset:59392
	s_waitcnt lgkmcnt(3)
	v_pk_fma_f32 v[168:169], v[68:69], v[224:225], v[168:169] op_sel_hi:[1,0,1]
	s_nop 0
	v_pk_fma_f32 v[164:165], v[70:71], v[224:225], v[168:169] op_sel:[0,1,0]
	s_nop 0
	v_pk_fma_f32 v[164:165], v[72:73], v[226:227], v[164:165] op_sel_hi:[1,0,1]
	v_mov_b32_e32 v166, v227
	v_pk_fma_f32 v[164:165], v[74:75], v[166:167], v[164:165] op_sel_hi:[1,0,1]
	ds_read_b128 v[240:243], v182 offset:60416
	s_waitcnt lgkmcnt(3)
	v_pk_fma_f32 v[170:171], v[124:125], v[228:229], 0 op_sel_hi:[1,0,0]
	s_nop 0
	v_pk_fma_f32 v[166:167], v[126:127], v[228:229], v[170:171] op_sel:[0,1,0]
	s_nop 0
	v_pk_fma_f32 v[166:167], v[128:129], v[230:231], v[166:167] op_sel_hi:[1,0,1]
	v_mov_b32_e32 v168, v231
	v_pk_fma_f32 v[170:171], v[130:131], v[168:169], v[166:167] op_sel_hi:[1,0,1]
	ds_read_b128 v[224:227], v182 offset:61440
	s_waitcnt lgkmcnt(3)
	v_pk_fma_f32 v[170:171], v[112:113], v[232:233], v[170:171] op_sel_hi:[1,0,1]
	s_nop 0
	v_pk_fma_f32 v[166:167], v[114:115], v[232:233], v[170:171] op_sel:[0,1,0]
	s_nop 0
	v_pk_fma_f32 v[166:167], v[118:119], v[234:235], v[166:167] op_sel_hi:[1,0,1]
	v_mov_b32_e32 v168, v235
	v_pk_fma_f32 v[170:171], v[122:123], v[168:169], v[166:167] op_sel_hi:[1,0,1]
	ds_read_b128 v[228:231], v182 offset:62464
	s_waitcnt lgkmcnt(3)
	v_pk_fma_f32 v[170:171], v[108:109], v[236:237], v[170:171] op_sel_hi:[1,0,1]
	s_nop 0
	v_pk_fma_f32 v[166:167], v[110:111], v[236:237], v[170:171] op_sel:[0,1,0]
	s_nop 0
	v_pk_fma_f32 v[166:167], v[116:117], v[238:239], v[166:167] op_sel_hi:[1,0,1]
	v_mov_b32_e32 v168, v239
	v_pk_fma_f32 v[170:171], v[120:121], v[168:169], v[166:167] op_sel_hi:[1,0,1]
	ds_read_b128 v[232:235], v182 offset:63488
	s_waitcnt lgkmcnt(3)
	v_pk_fma_f32 v[170:171], v[96:97], v[240:241], v[170:171] op_sel_hi:[1,0,1]
	s_nop 0
	v_pk_fma_f32 v[166:167], v[98:99], v[240:241], v[170:171] op_sel:[0,1,0]
	s_nop 0
	v_pk_fma_f32 v[166:167], v[102:103], v[242:243], v[166:167] op_sel_hi:[1,0,1]
	v_mov_b32_e32 v168, v243
	v_pk_fma_f32 v[170:171], v[106:107], v[168:169], v[166:167] op_sel_hi:[1,0,1]
	ds_read_b128 v[236:239], v182 offset:64512
	s_waitcnt lgkmcnt(3)
	v_pk_fma_f32 v[170:171], v[92:93], v[224:225], v[170:171] op_sel_hi:[1,0,1]
	s_nop 0
	v_pk_fma_f32 v[166:167], v[94:95], v[224:225], v[170:171] op_sel:[0,1,0]
	s_nop 0
	v_pk_fma_f32 v[166:167], v[100:101], v[226:227], v[166:167] op_sel_hi:[1,0,1]
	v_mov_b32_e32 v168, v227
	v_pk_fma_f32 v[170:171], v[104:105], v[168:169], v[166:167] op_sel_hi:[1,0,1]
	ds_read_b128 v[240:243], v244
	s_waitcnt lgkmcnt(3)
	v_pk_fma_f32 v[170:171], v[80:81], v[228:229], v[170:171] op_sel_hi:[1,0,1]
	s_nop 0
	v_pk_fma_f32 v[166:167], v[82:83], v[228:229], v[170:171] op_sel:[0,1,0]
	s_nop 0
	v_pk_fma_f32 v[166:167], v[86:87], v[230:231], v[166:167] op_sel_hi:[1,0,1]
	v_mov_b32_e32 v168, v231
	v_pk_fma_f32 v[170:171], v[90:91], v[168:169], v[166:167] op_sel_hi:[1,0,1]
	ds_read_b128 v[224:227], v244 offset:1024
	s_waitcnt lgkmcnt(3)
	v_pk_fma_f32 v[170:171], v[76:77], v[232:233], v[170:171] op_sel_hi:[1,0,1]
	s_nop 0
	v_pk_fma_f32 v[166:167], v[78:79], v[232:233], v[170:171] op_sel:[0,1,0]
	s_nop 0
	v_pk_fma_f32 v[166:167], v[84:85], v[234:235], v[166:167] op_sel_hi:[1,0,1]
	v_mov_b32_e32 v168, v235
	v_pk_fma_f32 v[170:171], v[88:89], v[168:169], v[166:167] op_sel_hi:[1,0,1]
	ds_read_b128 v[228:231], v244 offset:2048
	s_waitcnt lgkmcnt(3)
	v_pk_fma_f32 v[170:171], v[68:69], v[236:237], v[170:171] op_sel_hi:[1,0,1]
	s_nop 0
	v_pk_fma_f32 v[166:167], v[70:71], v[236:237], v[170:171] op_sel:[0,1,0]
	s_nop 0
	v_pk_fma_f32 v[166:167], v[72:73], v[238:239], v[166:167] op_sel_hi:[1,0,1]
	v_mov_b32_e32 v168, v239
	v_pk_fma_f32 v[166:167], v[74:75], v[168:169], v[166:167] op_sel_hi:[1,0,1]
	ds_read_b128 v[232:235], v244 offset:3072
	s_waitcnt lgkmcnt(3)
	v_pk_fma_f32 v[172:173], v[124:125], v[240:241], 0 op_sel_hi:[1,0,0]
	s_nop 0
	v_pk_fma_f32 v[168:169], v[126:127], v[240:241], v[172:173] op_sel:[0,1,0]
	s_nop 0
	v_pk_fma_f32 v[168:169], v[128:129], v[242:243], v[168:169] op_sel_hi:[1,0,1]
	v_mov_b32_e32 v170, v243
	v_pk_fma_f32 v[172:173], v[130:131], v[170:171], v[168:169] op_sel_hi:[1,0,1]
	ds_read_b128 v[236:239], v244 offset:4096
	s_waitcnt lgkmcnt(3)
	v_pk_fma_f32 v[172:173], v[112:113], v[224:225], v[172:173] op_sel_hi:[1,0,1]
	s_nop 0
	v_pk_fma_f32 v[168:169], v[114:115], v[224:225], v[172:173] op_sel:[0,1,0]
	s_nop 0
	v_pk_fma_f32 v[168:169], v[118:119], v[226:227], v[168:169] op_sel_hi:[1,0,1]
	v_mov_b32_e32 v170, v227
	v_pk_fma_f32 v[172:173], v[122:123], v[170:171], v[168:169] op_sel_hi:[1,0,1]
	ds_read_b128 v[240:243], v244 offset:5120
	s_waitcnt lgkmcnt(3)
	v_pk_fma_f32 v[172:173], v[108:109], v[228:229], v[172:173] op_sel_hi:[1,0,1]
	s_nop 0
	v_pk_fma_f32 v[168:169], v[110:111], v[228:229], v[172:173] op_sel:[0,1,0]
	s_nop 0
	v_pk_fma_f32 v[168:169], v[116:117], v[230:231], v[168:169] op_sel_hi:[1,0,1]
	v_mov_b32_e32 v170, v231
	v_pk_fma_f32 v[172:173], v[120:121], v[170:171], v[168:169] op_sel_hi:[1,0,1]
	ds_read_b128 v[224:227], v244 offset:6144
	s_waitcnt lgkmcnt(3)
	v_pk_fma_f32 v[172:173], v[96:97], v[232:233], v[172:173] op_sel_hi:[1,0,1]
	s_nop 0
	v_pk_fma_f32 v[168:169], v[98:99], v[232:233], v[172:173] op_sel:[0,1,0]
	s_nop 0
	v_pk_fma_f32 v[168:169], v[102:103], v[234:235], v[168:169] op_sel_hi:[1,0,1]
	v_mov_b32_e32 v170, v235
	v_pk_fma_f32 v[172:173], v[106:107], v[170:171], v[168:169] op_sel_hi:[1,0,1]
	ds_read_b128 v[228:231], v244 offset:7168
	s_waitcnt lgkmcnt(3)
; #define LAS __attribute__((address_space(3)))
; __device__ __forceinline__ void phase_norm2(const Params& p, const Ctx& F, const int l) {
;     ...
;         f32x2 lg[16];
;         unsigned wro = (unsigned)(uintptr_t)wr; asm volatile("" : "+v"(wro));
;         const LAS float* wr2 = (const LAS float*)(uintptr_t)wro;
; #pragma unroll
;         for (int e = 0; e < 16; ++e) { f32x2 a = {0.f, 0.f};
; #pragma unroll
;             for (int j = 0; j < 8; ++j) { const f32x4 w = *((const LAS f32x4*)(wr2 + e * DM) + F.lane + 64 * j);
; #pragma unroll
;                 for (int c = 0; c < 4; ++c) a += vv[j][c] * w[c]; }
;             lg[e] = a; }
	v_pk_fma_f32 v[172:173], v[92:93], v[236:237], v[172:173] op_sel_hi:[1,0,1]
	s_nop 0
	v_pk_fma_f32 v[168:169], v[94:95], v[236:237], v[172:173] op_sel:[0,1,0]
	s_nop 0
	v_pk_fma_f32 v[168:169], v[100:101], v[238:239], v[168:169] op_sel_hi:[1,0,1]
	v_mov_b32_e32 v170, v239
	v_pk_fma_f32 v[172:173], v[104:105], v[170:171], v[168:169] op_sel_hi:[1,0,1]
	ds_read_b128 v[232:235], v244 offset:8192
	s_waitcnt lgkmcnt(3)
	v_pk_fma_f32 v[172:173], v[80:81], v[240:241], v[172:173] op_sel_hi:[1,0,1]
	s_nop 0
	v_pk_fma_f32 v[168:169], v[82:83], v[240:241], v[172:173] op_sel:[0,1,0]
	s_nop 0
	v_pk_fma_f32 v[168:169], v[86:87], v[242:243], v[168:169] op_sel_hi:[1,0,1]
	v_mov_b32_e32 v170, v243
	v_pk_fma_f32 v[172:173], v[90:91], v[170:171], v[168:169] op_sel_hi:[1,0,1]
	ds_read_b128 v[236:239], v244 offset:9216
	s_waitcnt lgkmcnt(3)
	v_pk_fma_f32 v[172:173], v[76:77], v[224:225], v[172:173] op_sel_hi:[1,0,1]
	s_nop 0
	v_pk_fma_f32 v[168:169], v[78:79], v[224:225], v[172:173] op_sel:[0,1,0]
	s_nop 0
	v_pk_fma_f32 v[168:169], v[84:85], v[226:227], v[168:169] op_sel_hi:[1,0,1]
	v_mov_b32_e32 v170, v227
	v_pk_fma_f32 v[172:173], v[88:89], v[170:171], v[168:169] op_sel_hi:[1,0,1]
	ds_read_b128 v[240:243], v244 offset:10240
	s_waitcnt lgkmcnt(3)
	v_pk_fma_f32 v[172:173], v[68:69], v[228:229], v[172:173] op_sel_hi:[1,0,1]
	s_nop 0
	v_pk_fma_f32 v[168:169], v[70:71], v[228:229], v[172:173] op_sel:[0,1,0]
	s_nop 0
	v_pk_fma_f32 v[168:169], v[72:73], v[230:231], v[168:169] op_sel_hi:[1,0,1]
	v_mov_b32_e32 v170, v231
	v_pk_fma_f32 v[168:169], v[74:75], v[170:171], v[168:169] op_sel_hi:[1,0,1]
	ds_read_b128 v[224:227], v244 offset:11264
	s_waitcnt lgkmcnt(3)
	v_pk_fma_f32 v[174:175], v[124:125], v[232:233], 0 op_sel_hi:[1,0,0]
	s_nop 0
	v_pk_fma_f32 v[170:171], v[126:127], v[232:233], v[174:175] op_sel:[0,1,0]
	s_nop 0
	v_pk_fma_f32 v[170:171], v[128:129], v[234:235], v[170:171] op_sel_hi:[1,0,1]
	v_mov_b32_e32 v172, v235
	v_pk_fma_f32 v[174:175], v[130:131], v[172:173], v[170:171] op_sel_hi:[1,0,1]
	ds_read_b128 v[228:231], v244 offset:12288
	s_waitcnt lgkmcnt(3)
	v_pk_fma_f32 v[174:175], v[112:113], v[236:237], v[174:175] op_sel_hi:[1,0,1]
	s_nop 0
	v_pk_fma_f32 v[170:171], v[114:115], v[236:237], v[174:175] op_sel:[0,1,0]
	s_nop 0
	v_pk_fma_f32 v[170:171], v[118:119], v[238:239], v[170:171] op_sel_hi:[1,0,1]
	v_mov_b32_e32 v172, v239
	v_pk_fma_f32 v[174:175], v[122:123], v[172:173], v[170:171] op_sel_hi:[1,0,1]
	ds_read_b128 v[232:235], v244 offset:13312
	s_waitcnt lgkmcnt(3)
	v_pk_fma_f32 v[174:175], v[108:109], v[240:241], v[174:175] op_sel_hi:[1,0,1]
	s_nop 0
	v_pk_fma_f32 v[170:171], v[110:111], v[240:241], v[174:175] op_sel:[0,1,0]
	s_nop 0
	v_pk_fma_f32 v[170:171], v[116:117], v[242:243], v[170:171] op_sel_hi:[1,0,1]
	v_mov_b32_e32 v172, v243
	v_pk_fma_f32 v[174:175], v[120:121], v[172:173], v[170:171] op_sel_hi:[1,0,1]
	ds_read_b128 v[236:239], v244 offset:14336
	s_waitcnt lgkmcnt(3)
	v_pk_fma_f32 v[174:175], v[96:97], v[224:225], v[174:175] op_sel_hi:[1,0,1]
	s_nop 0
	v_pk_fma_f32 v[170:171], v[98:99], v[224:225], v[174:175] op_sel:[0,1,0]
	s_nop 0
	v_pk_fma_f32 v[170:171], v[102:103], v[226:227], v[170:171] op_sel_hi:[1,0,1]
	v_mov_b32_e32 v172, v227
	v_pk_fma_f32 v[174:175], v[106:107], v[172:173], v[170:171] op_sel_hi:[1,0,1]
	ds_read_b128 v[240:243], v244 offset:15360
	s_waitcnt lgkmcnt(3)
	v_pk_fma_f32 v[174:175], v[92:93], v[228:229], v[174:175] op_sel_hi:[1,0,1]
	s_nop 0
	v_pk_fma_f32 v[170:171], v[94:95], v[228:229], v[174:175] op_sel:[0,1,0]
	s_nop 0
	v_pk_fma_f32 v[170:171], v[100:101], v[230:231], v[170:171] op_sel_hi:[1,0,1]
	v_mov_b32_e32 v172, v231
	v_pk_fma_f32 v[174:175], v[104:105], v[172:173], v[170:171] op_sel_hi:[1,0,1]
	ds_read_b128 v[224:227], v244 offset:16384
	s_waitcnt lgkmcnt(3)
	v_pk_fma_f32 v[174:175], v[80:81], v[232:233], v[174:175] op_sel_hi:[1,0,1]
	s_nop 0
	v_pk_fma_f32 v[170:171], v[82:83], v[232:233], v[174:175] op_sel:[0,1,0]
	s_nop 0
	v_pk_fma_f32 v[170:171], v[86:87], v[234:235], v[170:171] op_sel_hi:[1,0,1]
	v_mov_b32_e32 v172, v235
	v_pk_fma_f32 v[174:175], v[90:91], v[172:173], v[170:171] op_sel_hi:[1,0,1]
	ds_read_b128 v[228:231], v244 offset:17408
	s_waitcnt lgkmcnt(3)
	v_pk_fma_f32 v[174:175], v[76:77], v[236:237], v[174:175] op_sel_hi:[1,0,1]
	s_nop 0
	v_pk_fma_f32 v[170:171], v[78:79], v[236:237], v[174:175] op_sel:[0,1,0]
	s_nop 0
	v_pk_fma_f32 v[170:171], v[84:85], v[238:239], v[170:171] op_sel_hi:[1,0,1]
	v_mov_b32_e32 v172, v239
	v_pk_fma_f32 v[174:175], v[88:89], v[172:173], v[170:171] op_sel_hi:[1,0,1]
	ds_read_b128 v[232:235], v244 offset:18432
	s_waitcnt lgkmcnt(3)
	v_pk_fma_f32 v[174:175], v[68:69], v[240:241], v[174:175] op_sel_hi:[1,0,1]
	s_nop 0
	v_pk_fma_f32 v[170:171], v[70:71], v[240:241], v[174:175] op_sel:[0,1,0]
	s_nop 0
	v_pk_fma_f32 v[170:171], v[72:73], v[242:243], v[170:171] op_sel_hi:[1,0,1]
	v_mov_b32_e32 v172, v243
	v_pk_fma_f32 v[170:171], v[74:75], v[172:173], v[170:171] op_sel_hi:[1,0,1]
	ds_read_b128 v[236:239], v244 offset:19456
	s_waitcnt lgkmcnt(3)
	v_pk_fma_f32 v[176:177], v[124:125], v[224:225], 0 op_sel_hi:[1,0,0]
	s_nop 0
	v_pk_fma_f32 v[172:173], v[126:127], v[224:225], v[176:177] op_sel:[0,1,0]
	s_nop 0
	v_pk_fma_f32 v[172:173], v[128:129], v[226:227], v[172:173] op_sel_hi:[1,0,1]
	v_mov_b32_e32 v174, v227
	v_pk_fma_f32 v[176:177], v[130:131], v[174:175], v[172:173] op_sel_hi:[1,0,1]
	ds_read_b128 v[240:243], v244 offset:20480
	s_waitcnt lgkmcnt(3)
	v_pk_fma_f32 v[176:177], v[112:113], v[228:229], v[176:177] op_sel_hi:[1,0,1]
	s_nop 0
	v_pk_fma_f32 v[172:173], v[114:115], v[228:229], v[176:177] op_sel:[0,1,0]
	s_nop 0
	v_pk_fma_f32 v[172:173], v[118:119], v[230:231], v[172:173] op_sel_hi:[1,0,1]
	v_mov_b32_e32 v174, v231
	v_pk_fma_f32 v[176:177], v[122:123], v[174:175], v[172:173] op_sel_hi:[1,0,1]
	ds_read_b128 v[224:227], v244 offset:21504
	s_waitcnt lgkmcnt(3)
; #define LAS __attribute__((address_space(3)))
; __device__ __forceinline__ void phase_norm2(const Params& p, const Ctx& F, const int l) {
;     ...
;         f32x2 lg[16];
;         unsigned wro = (unsigned)(uintptr_t)wr; asm volatile("" : "+v"(wro));
;         const LAS float* wr2 = (const LAS float*)(uintptr_t)wro;
; #pragma unroll
;         for (int e = 0; e < 16; ++e) { f32x2 a = {0.f, 0.f};
; #pragma unroll
;             for (int j = 0; j < 8; ++j) { const f32x4 w = *((const LAS f32x4*)(wr2 + e * DM) + F.lane + 64 * j);
; #pragma unroll
;                 for (int c = 0; c < 4; ++c) a += vv[j][c] * w[c]; }
;             lg[e] = a; }
	v_pk_fma_f32 v[176:177], v[108:109], v[232:233], v[176:177] op_sel_hi:[1,0,1]
	s_nop 0
	v_pk_fma_f32 v[172:173], v[110:111], v[232:233], v[176:177] op_sel:[0,1,0]
	s_nop 0
	v_pk_fma_f32 v[172:173], v[116:117], v[234:235], v[172:173] op_sel_hi:[1,0,1]
	v_mov_b32_e32 v174, v235
	v_pk_fma_f32 v[176:177], v[120:121], v[174:175], v[172:173] op_sel_hi:[1,0,1]
	ds_read_b128 v[228:231], v244 offset:22528
	s_waitcnt lgkmcnt(3)
	v_pk_fma_f32 v[176:177], v[96:97], v[236:237], v[176:177] op_sel_hi:[1,0,1]
	s_nop 0
	v_pk_fma_f32 v[172:173], v[98:99], v[236:237], v[176:177] op_sel:[0,1,0]
	s_nop 0
	v_pk_fma_f32 v[172:173], v[102:103], v[238:239], v[172:173] op_sel_hi:[1,0,1]
	v_mov_b32_e32 v174, v239
	v_pk_fma_f32 v[176:177], v[106:107], v[174:175], v[172:173] op_sel_hi:[1,0,1]
	ds_read_b128 v[232:235], v244 offset:23552
	s_waitcnt lgkmcnt(3)
	v_pk_fma_f32 v[176:177], v[92:93], v[240:241], v[176:177] op_sel_hi:[1,0,1]
	s_nop 0
	v_pk_fma_f32 v[172:173], v[94:95], v[240:241], v[176:177] op_sel:[0,1,0]
	s_nop 0
	v_pk_fma_f32 v[172:173], v[100:101], v[242:243], v[172:173] op_sel_hi:[1,0,1]
	v_mov_b32_e32 v174, v243
	v_pk_fma_f32 v[176:177], v[104:105], v[174:175], v[172:173] op_sel_hi:[1,0,1]
	ds_read_b128 v[236:239], v244 offset:24576
	s_waitcnt lgkmcnt(3)
	v_pk_fma_f32 v[176:177], v[80:81], v[224:225], v[176:177] op_sel_hi:[1,0,1]
	s_nop 0
	v_pk_fma_f32 v[172:173], v[82:83], v[224:225], v[176:177] op_sel:[0,1,0]
	s_nop 0
	v_pk_fma_f32 v[172:173], v[86:87], v[226:227], v[172:173] op_sel_hi:[1,0,1]
	v_mov_b32_e32 v174, v227
	v_pk_fma_f32 v[176:177], v[90:91], v[174:175], v[172:173] op_sel_hi:[1,0,1]
	ds_read_b128 v[240:243], v244 offset:25600
	s_waitcnt lgkmcnt(3)
	v_pk_fma_f32 v[176:177], v[76:77], v[228:229], v[176:177] op_sel_hi:[1,0,1]
	s_nop 0
	v_pk_fma_f32 v[172:173], v[78:79], v[228:229], v[176:177] op_sel:[0,1,0]
	s_nop 0
	v_pk_fma_f32 v[172:173], v[84:85], v[230:231], v[172:173] op_sel_hi:[1,0,1]
	v_mov_b32_e32 v174, v231
	v_pk_fma_f32 v[176:177], v[88:89], v[174:175], v[172:173] op_sel_hi:[1,0,1]
	ds_read_b128 v[224:227], v244 offset:26624
	s_waitcnt lgkmcnt(3)
	v_pk_fma_f32 v[176:177], v[68:69], v[232:233], v[176:177] op_sel_hi:[1,0,1]
	s_nop 0
	v_pk_fma_f32 v[172:173], v[70:71], v[232:233], v[176:177] op_sel:[0,1,0]
	s_nop 0
	v_pk_fma_f32 v[172:173], v[72:73], v[234:235], v[172:173] op_sel_hi:[1,0,1]
	v_mov_b32_e32 v174, v235
	v_pk_fma_f32 v[172:173], v[74:75], v[174:175], v[172:173] op_sel_hi:[1,0,1]
	ds_read_b128 v[228:231], v244 offset:27648
	s_waitcnt lgkmcnt(3)
	v_pk_fma_f32 v[178:179], v[124:125], v[236:237], 0 op_sel_hi:[1,0,0]
	s_nop 0
	v_pk_fma_f32 v[174:175], v[126:127], v[236:237], v[178:179] op_sel:[0,1,0]
	s_nop 0
	v_pk_fma_f32 v[174:175], v[128:129], v[238:239], v[174:175] op_sel_hi:[1,0,1]
	v_mov_b32_e32 v176, v239
	v_pk_fma_f32 v[178:179], v[130:131], v[176:177], v[174:175] op_sel_hi:[1,0,1]
	ds_read_b128 v[232:235], v244 offset:28672
	s_waitcnt lgkmcnt(3)
	v_pk_fma_f32 v[178:179], v[112:113], v[240:241], v[178:179] op_sel_hi:[1,0,1]
	s_nop 0
	v_pk_fma_f32 v[174:175], v[114:115], v[240:241], v[178:179] op_sel:[0,1,0]
	s_nop 0
	v_pk_fma_f32 v[174:175], v[118:119], v[242:243], v[174:175] op_sel_hi:[1,0,1]
	v_mov_b32_e32 v176, v243
	v_pk_fma_f32 v[178:179], v[122:123], v[176:177], v[174:175] op_sel_hi:[1,0,1]
	ds_read_b128 v[236:239], v244 offset:29696
	s_waitcnt lgkmcnt(3)
	v_pk_fma_f32 v[178:179], v[108:109], v[224:225], v[178:179] op_sel_hi:[1,0,1]
	s_nop 0
	v_pk_fma_f32 v[174:175], v[110:111], v[224:225], v[178:179] op_sel:[0,1,0]
	s_nop 0
	v_pk_fma_f32 v[174:175], v[116:117], v[226:227], v[174:175] op_sel_hi:[1,0,1]
	v_mov_b32_e32 v176, v227
	v_pk_fma_f32 v[178:179], v[120:121], v[176:177], v[174:175] op_sel_hi:[1,0,1]
	ds_read_b128 v[240:243], v244 offset:30720
	s_waitcnt lgkmcnt(3)
	v_pk_fma_f32 v[178:179], v[96:97], v[228:229], v[178:179] op_sel_hi:[1,0,1]
	s_nop 0
	v_pk_fma_f32 v[174:175], v[98:99], v[228:229], v[178:179] op_sel:[0,1,0]
	s_nop 0
	v_pk_fma_f32 v[174:175], v[102:103], v[230:231], v[174:175] op_sel_hi:[1,0,1]
	v_mov_b32_e32 v176, v231
	v_pk_fma_f32 v[178:179], v[106:107], v[176:177], v[174:175] op_sel_hi:[1,0,1]
	ds_read_b128 v[224:227], v244 offset:31744
	s_waitcnt lgkmcnt(3)
	v_pk_fma_f32 v[178:179], v[92:93], v[232:233], v[178:179] op_sel_hi:[1,0,1]
	s_nop 0
	v_pk_fma_f32 v[174:175], v[94:95], v[232:233], v[178:179] op_sel:[0,1,0]
	s_nop 0
	v_pk_fma_f32 v[174:175], v[100:101], v[234:235], v[174:175] op_sel_hi:[1,0,1]
	v_mov_b32_e32 v176, v235
	v_pk_fma_f32 v[178:179], v[104:105], v[176:177], v[174:175] op_sel_hi:[1,0,1]
	ds_read_b128 v[228:231], v244 offset:32768
	s_waitcnt lgkmcnt(3)
	v_pk_fma_f32 v[178:179], v[80:81], v[236:237], v[178:179] op_sel_hi:[1,0,1]
	s_nop 0
	v_pk_fma_f32 v[174:175], v[82:83], v[236:237], v[178:179] op_sel:[0,1,0]
	s_nop 0
	v_pk_fma_f32 v[174:175], v[86:87], v[238:239], v[174:175] op_sel_hi:[1,0,1]
	v_mov_b32_e32 v176, v239
	v_pk_fma_f32 v[178:179], v[90:91], v[176:177], v[174:175] op_sel_hi:[1,0,1]
	ds_read_b128 v[232:235], v244 offset:33792
	s_waitcnt lgkmcnt(3)
	v_pk_fma_f32 v[178:179], v[76:77], v[240:241], v[178:179] op_sel_hi:[1,0,1]
	s_nop 0
	v_pk_fma_f32 v[174:175], v[78:79], v[240:241], v[178:179] op_sel:[0,1,0]
	s_nop 0
	v_pk_fma_f32 v[174:175], v[84:85], v[242:243], v[174:175] op_sel_hi:[1,0,1]
	v_mov_b32_e32 v176, v243
	v_pk_fma_f32 v[178:179], v[88:89], v[176:177], v[174:175] op_sel_hi:[1,0,1]
	ds_read_b128 v[236:239], v244 offset:34816
	s_waitcnt lgkmcnt(3)
; #define LAS __attribute__((address_space(3)))
; __device__ __forceinline__ void phase_norm2(const Params& p, const Ctx& F, const int l) {
;     ...
;         f32x2 lg[16];
;         unsigned wro = (unsigned)(uintptr_t)wr; asm volatile("" : "+v"(wro));
;         const LAS float* wr2 = (const LAS float*)(uintptr_t)wro;
; #pragma unroll
;         for (int e = 0; e < 16; ++e) { f32x2 a = {0.f, 0.f};
; #pragma unroll
;             for (int j = 0; j < 8; ++j) { const f32x4 w = *((const LAS f32x4*)(wr2 + e * DM) + F.lane + 64 * j);
; #pragma unroll
;                 for (int c = 0; c < 4; ++c) a += vv[j][c] * w[c]; }
;             lg[e] = a; }
	v_pk_fma_f32 v[178:179], v[68:69], v[224:225], v[178:179] op_sel_hi:[1,0,1]
	s_nop 0
	v_pk_fma_f32 v[174:175], v[70:71], v[224:225], v[178:179] op_sel:[0,1,0]
	s_nop 0
	v_pk_fma_f32 v[174:175], v[72:73], v[226:227], v[174:175] op_sel_hi:[1,0,1]
	v_mov_b32_e32 v176, v227
	v_pk_fma_f32 v[174:175], v[74:75], v[176:177], v[174:175] op_sel_hi:[1,0,1]
	ds_read_b128 v[240:243], v244 offset:35840
	s_waitcnt lgkmcnt(3)
	v_pk_fma_f32 v[180:181], v[124:125], v[228:229], 0 op_sel_hi:[1,0,0]
	s_nop 0
	v_pk_fma_f32 v[176:177], v[126:127], v[228:229], v[180:181] op_sel:[0,1,0]
	s_nop 0
	v_pk_fma_f32 v[176:177], v[128:129], v[230:231], v[176:177] op_sel_hi:[1,0,1]
	v_mov_b32_e32 v178, v231
	v_pk_fma_f32 v[180:181], v[130:131], v[178:179], v[176:177] op_sel_hi:[1,0,1]
	ds_read_b128 v[224:227], v244 offset:36864
	s_waitcnt lgkmcnt(3)
	v_pk_fma_f32 v[180:181], v[112:113], v[232:233], v[180:181] op_sel_hi:[1,0,1]
	s_nop 0
	v_pk_fma_f32 v[176:177], v[114:115], v[232:233], v[180:181] op_sel:[0,1,0]
	s_nop 0
	v_pk_fma_f32 v[176:177], v[118:119], v[234:235], v[176:177] op_sel_hi:[1,0,1]
	v_mov_b32_e32 v178, v235
	v_pk_fma_f32 v[180:181], v[122:123], v[178:179], v[176:177] op_sel_hi:[1,0,1]
	ds_read_b128 v[228:231], v244 offset:37888
	s_waitcnt lgkmcnt(3)
	v_pk_fma_f32 v[180:181], v[108:109], v[236:237], v[180:181] op_sel_hi:[1,0,1]
	s_nop 0
	v_pk_fma_f32 v[176:177], v[110:111], v[236:237], v[180:181] op_sel:[0,1,0]
	s_nop 0
	v_pk_fma_f32 v[176:177], v[116:117], v[238:239], v[176:177] op_sel_hi:[1,0,1]
	v_mov_b32_e32 v178, v239
	v_pk_fma_f32 v[180:181], v[120:121], v[178:179], v[176:177] op_sel_hi:[1,0,1]
	ds_read_b128 v[232:235], v244 offset:38912
	s_waitcnt lgkmcnt(3)
	v_pk_fma_f32 v[180:181], v[96:97], v[240:241], v[180:181] op_sel_hi:[1,0,1]
	s_nop 0
	v_pk_fma_f32 v[176:177], v[98:99], v[240:241], v[180:181] op_sel:[0,1,0]
	s_nop 0
	v_pk_fma_f32 v[176:177], v[102:103], v[242:243], v[176:177] op_sel_hi:[1,0,1]
	v_mov_b32_e32 v178, v243
	v_pk_fma_f32 v[180:181], v[106:107], v[178:179], v[176:177] op_sel_hi:[1,0,1]
	ds_read_b128 v[236:239], v244 offset:39936
	s_waitcnt lgkmcnt(3)
	v_pk_fma_f32 v[180:181], v[92:93], v[224:225], v[180:181] op_sel_hi:[1,0,1]
	s_nop 0
	v_pk_fma_f32 v[176:177], v[94:95], v[224:225], v[180:181] op_sel:[0,1,0]
	s_nop 0
	v_pk_fma_f32 v[176:177], v[100:101], v[226:227], v[176:177] op_sel_hi:[1,0,1]
	v_mov_b32_e32 v178, v227
	v_pk_fma_f32 v[180:181], v[104:105], v[178:179], v[176:177] op_sel_hi:[1,0,1]
	ds_read_b128 v[240:243], v244 offset:40960
	s_waitcnt lgkmcnt(3)
	v_pk_fma_f32 v[180:181], v[80:81], v[228:229], v[180:181] op_sel_hi:[1,0,1]
	s_nop 0
	v_pk_fma_f32 v[176:177], v[82:83], v[228:229], v[180:181] op_sel:[0,1,0]
	s_nop 0
	v_pk_fma_f32 v[176:177], v[86:87], v[230:231], v[176:177] op_sel_hi:[1,0,1]
	v_mov_b32_e32 v178, v231
	v_pk_fma_f32 v[180:181], v[90:91], v[178:179], v[176:177] op_sel_hi:[1,0,1]
	ds_read_b128 v[224:227], v244 offset:41984
	s_waitcnt lgkmcnt(3)
	v_pk_fma_f32 v[180:181], v[76:77], v[232:233], v[180:181] op_sel_hi:[1,0,1]
	s_nop 0
	v_pk_fma_f32 v[176:177], v[78:79], v[232:233], v[180:181] op_sel:[0,1,0]
	s_nop 0
	v_pk_fma_f32 v[176:177], v[84:85], v[234:235], v[176:177] op_sel_hi:[1,0,1]
	v_mov_b32_e32 v178, v235
	v_pk_fma_f32 v[180:181], v[88:89], v[178:179], v[176:177] op_sel_hi:[1,0,1]
	ds_read_b128 v[228:231], v244 offset:43008
	s_waitcnt lgkmcnt(3)
	v_pk_fma_f32 v[180:181], v[68:69], v[236:237], v[180:181] op_sel_hi:[1,0,1]
	s_nop 0
	v_pk_fma_f32 v[176:177], v[70:71], v[236:237], v[180:181] op_sel:[0,1,0]
	s_nop 0
	v_pk_fma_f32 v[176:177], v[72:73], v[238:239], v[176:177] op_sel_hi:[1,0,1]
	v_mov_b32_e32 v178, v239
	v_pk_fma_f32 v[176:177], v[74:75], v[178:179], v[176:177] op_sel_hi:[1,0,1]
	ds_read_b128 v[232:235], v244 offset:44032
	s_waitcnt lgkmcnt(3)
	v_pk_fma_f32 v[184:185], v[124:125], v[240:241], 0 op_sel_hi:[1,0,0]
	s_nop 0
	v_pk_fma_f32 v[178:179], v[126:127], v[240:241], v[184:185] op_sel:[0,1,0]
	s_nop 0
	v_pk_fma_f32 v[178:179], v[128:129], v[242:243], v[178:179] op_sel_hi:[1,0,1]
	v_mov_b32_e32 v180, v243
	v_pk_fma_f32 v[184:185], v[130:131], v[180:181], v[178:179] op_sel_hi:[1,0,1]
	ds_read_b128 v[236:239], v244 offset:45056
	s_waitcnt lgkmcnt(3)
	v_pk_fma_f32 v[184:185], v[112:113], v[224:225], v[184:185] op_sel_hi:[1,0,1]
	s_nop 0
	v_pk_fma_f32 v[178:179], v[114:115], v[224:225], v[184:185] op_sel:[0,1,0]
	s_nop 0
	v_pk_fma_f32 v[178:179], v[118:119], v[226:227], v[178:179] op_sel_hi:[1,0,1]
	v_mov_b32_e32 v180, v227
	v_pk_fma_f32 v[184:185], v[122:123], v[180:181], v[178:179] op_sel_hi:[1,0,1]
	ds_read_b128 v[240:243], v244 offset:46080
	s_waitcnt lgkmcnt(3)
	v_pk_fma_f32 v[184:185], v[108:109], v[228:229], v[184:185] op_sel_hi:[1,0,1]
	s_nop 0
	v_pk_fma_f32 v[178:179], v[110:111], v[228:229], v[184:185] op_sel:[0,1,0]
	s_nop 0
	v_pk_fma_f32 v[178:179], v[116:117], v[230:231], v[178:179] op_sel_hi:[1,0,1]
	v_mov_b32_e32 v180, v231
	v_pk_fma_f32 v[184:185], v[120:121], v[180:181], v[178:179] op_sel_hi:[1,0,1]
	ds_read_b128 v[224:227], v244 offset:47104
	s_waitcnt lgkmcnt(3)
	v_pk_fma_f32 v[184:185], v[96:97], v[232:233], v[184:185] op_sel_hi:[1,0,1]
	s_nop 0
	v_pk_fma_f32 v[178:179], v[98:99], v[232:233], v[184:185] op_sel:[0,1,0]
	s_nop 0
	v_pk_fma_f32 v[178:179], v[102:103], v[234:235], v[178:179] op_sel_hi:[1,0,1]
	v_mov_b32_e32 v180, v235
	v_pk_fma_f32 v[184:185], v[106:107], v[180:181], v[178:179] op_sel_hi:[1,0,1]
	ds_read_b128 v[228:231], v244 offset:48128
	s_waitcnt lgkmcnt(3)
; #define LAS __attribute__((address_space(3)))
; __device__ __forceinline__ void phase_norm2(const Params& p, const Ctx& F, const int l) {
;     ...
;         f32x2 lg[16];
;         unsigned wro = (unsigned)(uintptr_t)wr; asm volatile("" : "+v"(wro));
;         const LAS float* wr2 = (const LAS float*)(uintptr_t)wro;
; #pragma unroll
;         for (int e = 0; e < 16; ++e) { f32x2 a = {0.f, 0.f};
; #pragma unroll
;             for (int j = 0; j < 8; ++j) { const f32x4 w = *((const LAS f32x4*)(wr2 + e * DM) + F.lane + 64 * j);
; #pragma unroll
;                 for (int c = 0; c < 4; ++c) a += vv[j][c] * w[c]; }
;             lg[e] = a; }
	v_pk_fma_f32 v[184:185], v[92:93], v[236:237], v[184:185] op_sel_hi:[1,0,1]
	s_nop 0
	v_pk_fma_f32 v[178:179], v[94:95], v[236:237], v[184:185] op_sel:[0,1,0]
	s_nop 0
	v_pk_fma_f32 v[178:179], v[100:101], v[238:239], v[178:179] op_sel_hi:[1,0,1]
	v_mov_b32_e32 v180, v239
	v_pk_fma_f32 v[184:185], v[104:105], v[180:181], v[178:179] op_sel_hi:[1,0,1]
	ds_read_b128 v[232:235], v244 offset:49152
	s_waitcnt lgkmcnt(3)
	v_pk_fma_f32 v[184:185], v[80:81], v[240:241], v[184:185] op_sel_hi:[1,0,1]
	s_nop 0
	v_pk_fma_f32 v[178:179], v[82:83], v[240:241], v[184:185] op_sel:[0,1,0]
	s_nop 0
	v_pk_fma_f32 v[178:179], v[86:87], v[242:243], v[178:179] op_sel_hi:[1,0,1]
	v_mov_b32_e32 v180, v243
	v_pk_fma_f32 v[184:185], v[90:91], v[180:181], v[178:179] op_sel_hi:[1,0,1]
	ds_read_b128 v[236:239], v244 offset:50176
	s_waitcnt lgkmcnt(3)
	v_pk_fma_f32 v[184:185], v[76:77], v[224:225], v[184:185] op_sel_hi:[1,0,1]
	s_nop 0
	v_pk_fma_f32 v[178:179], v[78:79], v[224:225], v[184:185] op_sel:[0,1,0]
	s_nop 0
	v_pk_fma_f32 v[178:179], v[84:85], v[226:227], v[178:179] op_sel_hi:[1,0,1]
	v_mov_b32_e32 v180, v227
	v_pk_fma_f32 v[184:185], v[88:89], v[180:181], v[178:179] op_sel_hi:[1,0,1]
	ds_read_b128 v[240:243], v244 offset:51200
	s_waitcnt lgkmcnt(3)
	v_pk_fma_f32 v[184:185], v[68:69], v[228:229], v[184:185] op_sel_hi:[1,0,1]
	s_nop 0
	v_pk_fma_f32 v[178:179], v[70:71], v[228:229], v[184:185] op_sel:[0,1,0]
	ds_read_b128 v[224:227], v244 offset:52224
	v_pk_fma_f32 v[178:179], v[72:73], v[230:231], v[178:179] op_sel_hi:[1,0,1]
	v_mov_b32_e32 v180, v231
	v_pk_fma_f32 v[178:179], v[74:75], v[180:181], v[178:179] op_sel_hi:[1,0,1]
	s_waitcnt lgkmcnt(3)
	v_pk_fma_f32 v[180:181], v[124:125], v[232:233], 0 op_sel_hi:[1,0,0]
	s_nop 0
	v_pk_fma_f32 v[180:181], v[126:127], v[232:233], v[180:181] op_sel:[0,1,0]
	v_mov_b32_e32 v184, v235
	v_pk_fma_f32 v[180:181], v[128:129], v[234:235], v[180:181] op_sel_hi:[1,0,1]
	s_nop 0
	v_pk_fma_f32 v[180:181], v[130:131], v[184:185], v[180:181] op_sel_hi:[1,0,1]
	ds_read_b128 v[228:231], v244 offset:53248
	s_waitcnt lgkmcnt(3)
	v_pk_fma_f32 v[180:181], v[112:113], v[236:237], v[180:181] op_sel_hi:[1,0,1]
	s_nop 0
	v_pk_fma_f32 v[180:181], v[114:115], v[236:237], v[180:181] op_sel:[0,1,0]
	v_mov_b32_e32 v184, v239
	v_pk_fma_f32 v[180:181], v[118:119], v[238:239], v[180:181] op_sel_hi:[1,0,1]
	s_nop 0
	v_pk_fma_f32 v[180:181], v[122:123], v[184:185], v[180:181] op_sel_hi:[1,0,1]
	ds_read_b128 v[232:235], v244 offset:54272
	s_waitcnt lgkmcnt(3)
	v_pk_fma_f32 v[180:181], v[108:109], v[240:241], v[180:181] op_sel_hi:[1,0,1]
	s_nop 0
	v_pk_fma_f32 v[180:181], v[110:111], v[240:241], v[180:181] op_sel:[0,1,0]
	v_mov_b32_e32 v184, v243
	v_pk_fma_f32 v[180:181], v[116:117], v[242:243], v[180:181] op_sel_hi:[1,0,1]
	s_nop 0
	v_pk_fma_f32 v[180:181], v[120:121], v[184:185], v[180:181] op_sel_hi:[1,0,1]
	ds_read_b128 v[236:239], v244 offset:55296
	s_waitcnt lgkmcnt(3)
	v_pk_fma_f32 v[180:181], v[96:97], v[224:225], v[180:181] op_sel_hi:[1,0,1]
	s_nop 0
	v_pk_fma_f32 v[180:181], v[98:99], v[224:225], v[180:181] op_sel:[0,1,0]
	v_mov_b32_e32 v184, v227
	v_pk_fma_f32 v[180:181], v[102:103], v[226:227], v[180:181] op_sel_hi:[1,0,1]
	s_nop 0
	v_pk_fma_f32 v[180:181], v[106:107], v[184:185], v[180:181] op_sel_hi:[1,0,1]
	ds_read_b128 v[240:243], v244 offset:56320
	s_waitcnt lgkmcnt(3)
	v_pk_fma_f32 v[180:181], v[92:93], v[228:229], v[180:181] op_sel_hi:[1,0,1]
	s_nop 0
	v_pk_fma_f32 v[180:181], v[94:95], v[228:229], v[180:181] op_sel:[0,1,0]
	v_mov_b32_e32 v184, v231
	v_pk_fma_f32 v[180:181], v[100:101], v[230:231], v[180:181] op_sel_hi:[1,0,1]
	s_nop 0
	v_pk_fma_f32 v[180:181], v[104:105], v[184:185], v[180:181] op_sel_hi:[1,0,1]
	ds_read_b128 v[224:227], v244 offset:57344
	s_waitcnt lgkmcnt(3)
	v_pk_fma_f32 v[180:181], v[80:81], v[232:233], v[180:181] op_sel_hi:[1,0,1]
	s_nop 0
	v_pk_fma_f32 v[180:181], v[82:83], v[232:233], v[180:181] op_sel:[0,1,0]
	v_mov_b32_e32 v184, v235
	v_pk_fma_f32 v[180:181], v[86:87], v[234:235], v[180:181] op_sel_hi:[1,0,1]
	s_nop 0
	v_pk_fma_f32 v[180:181], v[90:91], v[184:185], v[180:181] op_sel_hi:[1,0,1]
	ds_read_b128 v[228:231], v244 offset:58368
	s_waitcnt lgkmcnt(3)
	v_pk_fma_f32 v[180:181], v[76:77], v[236:237], v[180:181] op_sel_hi:[1,0,1]
	s_nop 0
	v_pk_fma_f32 v[180:181], v[78:79], v[236:237], v[180:181] op_sel:[0,1,0]
	v_mov_b32_e32 v184, v239
	v_pk_fma_f32 v[180:181], v[84:85], v[238:239], v[180:181] op_sel_hi:[1,0,1]
	s_nop 0
	v_pk_fma_f32 v[180:181], v[88:89], v[184:185], v[180:181] op_sel_hi:[1,0,1]
	ds_read_b128 v[232:235], v244 offset:59392
	s_waitcnt lgkmcnt(3)
	v_pk_fma_f32 v[180:181], v[68:69], v[240:241], v[180:181] op_sel_hi:[1,0,1]
	s_nop 0
	v_pk_fma_f32 v[180:181], v[70:71], v[240:241], v[180:181] op_sel:[0,1,0]
	v_mov_b32_e32 v184, v243
	v_pk_fma_f32 v[180:181], v[72:73], v[242:243], v[180:181] op_sel_hi:[1,0,1]
	s_nop 0
	v_pk_fma_f32 v[180:181], v[74:75], v[184:185], v[180:181] op_sel_hi:[1,0,1]
	ds_read_b128 v[236:239], v244 offset:60416
	s_waitcnt lgkmcnt(3)
	v_pk_fma_f32 v[124:125], v[124:125], v[224:225], 0 op_sel_hi:[1,0,0]
	s_nop 0
	v_pk_fma_f32 v[124:125], v[126:127], v[224:225], v[124:125] op_sel:[0,1,0]
	v_mov_b32_e32 v126, v227
	v_pk_fma_f32 v[124:125], v[128:129], v[226:227], v[124:125] op_sel_hi:[1,0,1]
	s_nop 0
	v_pk_fma_f32 v[128:129], v[130:131], v[126:127], v[124:125] op_sel_hi:[1,0,1]
	ds_read_b128 v[240:243], v244 offset:61440
	s_waitcnt lgkmcnt(3)
	v_pk_fma_f32 v[112:113], v[112:113], v[228:229], v[128:129] op_sel_hi:[1,0,1]
	s_nop 0
	v_pk_fma_f32 v[112:113], v[114:115], v[228:229], v[112:113] op_sel:[0,1,0]
	v_mov_b32_e32 v114, v231
	v_pk_fma_f32 v[112:113], v[118:119], v[230:231], v[112:113] op_sel_hi:[1,0,1]
	s_nop 0
	v_pk_fma_f32 v[118:119], v[122:123], v[114:115], v[112:113] op_sel_hi:[1,0,1]
	ds_read_b128 v[224:227], v244 offset:62464
	s_waitcnt lgkmcnt(3)
; #define LAS __attribute__((address_space(3)))
; __device__ __forceinline__ void router_tail(const Ctx& F, const float (&lg)[16], const int b, const int t, const bool valid) {
;     const bool b5 = (F.lane & 32) != 0, b4 = (F.lane & 16) != 0, b3 = (F.lane & 8) != 0, b2 = (F.lane & 4) != 0;
;     float r8[8], r4[4], r2[2];
; #pragma unroll
;     for (int e = 0; e < 8; ++e) { const float keep = b5 ? lg[e + 8] : lg[e], send = b5 ? lg[e] : lg[e + 8]; r8[e] = keep + __shfl_xor(send, 32); }
; #pragma unroll
;     for (int e = 0; e < 4; ++e) { const float keep = b4 ? r8[e + 4] : r8[e], send = b4 ? r8[e] : r8[e + 4]; r4[e] = keep + __shfl_xor(send, 16); }
; #pragma unroll
;     for (int e = 0; e < 2; ++e) { const float keep = b3 ? r4[e + 2] : r4[e], send = b3 ? r4[e] : r4[e + 2]; r2[e] = keep + __shfl_xor(send, 8); }
;     float lgt; { const float keep = b2 ? r2[1] : r2[0], send = b2 ? r2[0] : r2[1]; lgt = keep + __shfl_xor(send, 4); }
;     lgt += __shfl_xor(lgt, 2); lgt += __shfl_xor(lgt, 1);
;     float mx = lgt;
;     mx = fmaxf(mx, __shfl_xor(mx, 4)); mx = fmaxf(mx, __shfl_xor(mx, 8)); mx = fmaxf(mx, __shfl_xor(mx, 16)); mx = fmaxf(mx, __shfl_xor(mx, 32));
;     const float ex = expf(lgt - mx); float sum = ex;
;     sum += __shfl_xor(sum, 4); sum += __shfl_xor(sum, 8); sum += __shfl_xor(sum, 16); sum += __shfl_xor(sum, 32);
;     if (valid && (F.lane & 3) == 0) { const float af = ex / sum; const int e = F.lane >> 2;
;         if (t < CTXL) F.affc[((size_t)(b * 16 + e)) * CTXL + t] = af; else F.affl[((size_t)(b * 16 + e)) * SEQ + (t - CTXL)] = af; }
; __device__ __forceinline__ void phase_norm2(const Params& p, const Ctx& F, const int l) {
;     ...
;         for (int e = 0; e < 16; ++e) { f32x2 a = {0.f, 0.f};
; #pragma unroll
;             for (int j = 0; j < 8; ++j) { const f32x4 w = *((const LAS f32x4*)(wr2 + e * DM) + F.lane + 64 * j);
; #pragma unroll
;                 for (int c = 0; c < 4; ++c) a += vv[j][c] * w[c]; }
;             lg[e] = a; }
	v_pk_fma_f32 v[108:109], v[108:109], v[232:233], v[118:119] op_sel_hi:[1,0,1]
	s_nop 0
	v_pk_fma_f32 v[108:109], v[110:111], v[232:233], v[108:109] op_sel:[0,1,0]
	v_mov_b32_e32 v110, v235
	v_pk_fma_f32 v[108:109], v[116:117], v[234:235], v[108:109] op_sel_hi:[1,0,1]
	s_nop 0
	v_pk_fma_f32 v[112:113], v[120:121], v[110:111], v[108:109] op_sel_hi:[1,0,1]
	ds_read_b128 v[228:231], v244 offset:63488
	s_waitcnt lgkmcnt(3)
	v_pk_fma_f32 v[96:97], v[96:97], v[236:237], v[112:113] op_sel_hi:[1,0,1]
	s_nop 0
	v_pk_fma_f32 v[96:97], v[98:99], v[236:237], v[96:97] op_sel:[0,1,0]
	v_mov_b32_e32 v98, v239
	v_pk_fma_f32 v[96:97], v[102:103], v[238:239], v[96:97] op_sel_hi:[1,0,1]
	s_nop 0
	v_pk_fma_f32 v[102:103], v[106:107], v[98:99], v[96:97] op_sel_hi:[1,0,1]
	ds_read_b128 v[232:235], v244 offset:64512
	s_waitcnt lgkmcnt(3)
	v_pk_fma_f32 v[92:93], v[92:93], v[240:241], v[102:103] op_sel_hi:[1,0,1]
	s_nop 0
	v_pk_fma_f32 v[92:93], v[94:95], v[240:241], v[92:93] op_sel:[0,1,0]
	v_mov_b32_e32 v94, v243
	v_pk_fma_f32 v[92:93], v[100:101], v[242:243], v[92:93] op_sel_hi:[1,0,1]
	s_nop 0
	v_pk_fma_f32 v[96:97], v[104:105], v[94:95], v[92:93] op_sel_hi:[1,0,1]
	s_waitcnt lgkmcnt(2)
	v_pk_fma_f32 v[80:81], v[80:81], v[224:225], v[96:97] op_sel_hi:[1,0,1]
	s_nop 0
	v_pk_fma_f32 v[80:81], v[82:83], v[224:225], v[80:81] op_sel:[0,1,0]
	v_mov_b32_e32 v82, v227
	v_pk_fma_f32 v[80:81], v[86:87], v[226:227], v[80:81] op_sel_hi:[1,0,1]
	s_nop 0
	v_pk_fma_f32 v[86:87], v[90:91], v[82:83], v[80:81] op_sel_hi:[1,0,1]
	s_waitcnt lgkmcnt(1)
	v_pk_fma_f32 v[76:77], v[76:77], v[228:229], v[86:87] op_sel_hi:[1,0,1]
	s_nop 0
	v_pk_fma_f32 v[76:77], v[78:79], v[228:229], v[76:77] op_sel:[0,1,0]
	v_mov_b32_e32 v78, v231
	v_pk_fma_f32 v[76:77], v[84:85], v[230:231], v[76:77] op_sel_hi:[1,0,1]
	s_nop 0
	v_pk_fma_f32 v[80:81], v[88:89], v[78:79], v[76:77] op_sel_hi:[1,0,1]
	v_cndmask_b32_e64 v1, v168, v152, s[38:39]
	s_waitcnt lgkmcnt(0)
	v_pk_fma_f32 v[68:69], v[68:69], v[232:233], v[80:81] op_sel_hi:[1,0,1]
	s_nop 0
	v_pk_fma_f32 v[68:69], v[70:71], v[232:233], v[68:69] op_sel:[0,1,0]
	v_mov_b32_e32 v70, v235
	v_pk_fma_f32 v[68:69], v[72:73], v[234:235], v[68:69] op_sel_hi:[1,0,1]
	v_cndmask_b32_e64 v72, v156, v172, s[38:39]
	v_pk_fma_f32 v[68:69], v[74:75], v[70:71], v[68:69] op_sel_hi:[1,0,1]
	s_nop 1
	v_permlane32_swap_b32_e32 v152, v168
	v_permlane32_swap_b32_e32 v154, v170
	v_permlane32_swap_b32_e32 v156, v172
	v_permlane32_swap_b32_e32 v158, v174
	v_permlane32_swap_b32_e32 v160, v176
	v_permlane32_swap_b32_e32 v162, v178
	v_permlane32_swap_b32_e32 v164, v180
	v_permlane32_swap_b32_e32 v166, v68
	v_add_f32_e32 v1, v152, v168
	v_add_f32_e32 v70, v154, v170
	v_add_f32_e32 v71, v156, v172
	v_add_f32_e32 v72, v158, v174
	v_add_f32_e32 v73, v160, v176
	v_add_f32_e32 v74, v162, v178
	v_add_f32_e32 v75, v164, v180
	v_add_f32_e32 v68, v166, v68
	s_waitcnt lgkmcnt(0)
	v_cndmask_b32_e64 v76, v73, v1, s[40:41]
	v_cndmask_b32_e64 v1, v1, v73, s[40:41]
	v_cndmask_b32_e64 v73, v74, v70, s[40:41]
	v_cndmask_b32_e64 v70, v70, v74, s[40:41]
	ds_bpermute_b32 v70, v193, v70
	ds_bpermute_b32 v1, v193, v1
	s_waitcnt lgkmcnt(1)
	v_add_f32_e32 v70, v73, v70
	v_cndmask_b32_e64 v73, v75, v71, s[40:41]
	v_cndmask_b32_e64 v71, v71, v75, s[40:41]
	ds_bpermute_b32 v71, v193, v71
	s_waitcnt lgkmcnt(1)
	v_add_f32_e32 v1, v76, v1
	s_waitcnt lgkmcnt(0)
	v_add_f32_e32 v71, v73, v71
	v_cndmask_b32_e64 v73, v68, v72, s[40:41]
	v_cndmask_b32_e64 v68, v72, v68, s[40:41]
	ds_bpermute_b32 v68, v193, v68
	v_cndmask_b32_e64 v72, v71, v1, s[42:43]
	v_cndmask_b32_e64 v1, v1, v71, s[42:43]
	ds_bpermute_b32 v1, v192, v1
	s_waitcnt lgkmcnt(1)
	v_add_f32_e32 v68, v73, v68
	v_cndmask_b32_e64 v71, v68, v70, s[42:43]
	v_cndmask_b32_e64 v68, v70, v68, s[42:43]
	ds_bpermute_b32 v68, v192, v68
	s_waitcnt lgkmcnt(1)
	v_add_f32_e32 v1, v72, v1
	s_waitcnt lgkmcnt(0)
	v_add_f32_e32 v68, v71, v68
	v_cndmask_b32_e64 v70, v68, v1, s[4:5]
	v_cndmask_b32_e64 v1, v1, v68, s[4:5]
	ds_bpermute_b32 v1, v191, v1
	s_waitcnt lgkmcnt(0)
	v_add_f32_e32 v1, v70, v1
	s_nop 1
	v_add_f32_dpp v1, v1, v1 quad_perm:[2,3,0,1] row_mask:0xf bank_mask:0xf
	s_nop 1
	v_add_f32_dpp v1, v1, v1 quad_perm:[1,0,3,2] row_mask:0xf bank_mask:0xf
	s_nop 1
	v_max_f32_dpp v68, v1, v1 row_half_mirror row_mask:0xf bank_mask:0xf
	s_nop 1
	v_max_f32_dpp v68, v68, v68 row_mirror row_mask:0xf bank_mask:0xf
	v_mov_b32_e32 v70, v68
	s_nop 1
	v_permlane16_swap_b32_e32 v68, v70
	v_max_f32_e32 v68, v68, v70
	v_mov_b32_e32 v70, v68
	s_nop 1
	v_permlane32_swap_b32_e32 v68, v70
	v_max_f32_e32 v68, v68, v70
	v_sub_f32_e32 v1, v1, v68
	v_mul_f32_e32 v68, 0x3fb8aa3b, v1
	v_fma_f32 v70, v1, s55, -v68
	v_rndne_f32_e32 v71, v68
	v_fmac_f32_e32 v70, 0x32a5705f, v1
	v_sub_f32_e32 v68, v68, v71
	v_add_f32_e32 v68, v68, v70
	v_exp_f32_e32 v68, v68
	v_cvt_i32_f32_e32 v70, v71
	v_cmp_ngt_f32_e32 vcc, s56, v1
	v_ldexp_f32 v68, v68, v70
	s_nop 0
	v_cndmask_b32_e32 v68, 0, v68, vcc
	v_cmp_nlt_f32_e32 vcc, s57, v1
	s_nop 1
	v_cndmask_b32_e32 v68, v222, v68, vcc
	s_nop 1
	v_add_f32_dpp v1, v68, v68 row_half_mirror row_mask:0xf bank_mask:0xf
	s_nop 1
	v_add_f32_dpp v1, v1, v1 row_mirror row_mask:0xf bank_mask:0xf
	v_mov_b32_e32 v70, v1
	s_nop 1
	v_permlane16_swap_b32_e32 v1, v70
	v_add_f32_e32 v70, v1, v70
	ds_bpermute_b32 v71, v194, v70
	s_and_saveexec_b64 s[0:1], s[6:7]
	s_cbranch_execz .LBB0_942
	s_waitcnt lgkmcnt(0)
	v_add_f32_e32 v1, v70, v71
	v_div_scale_f32 v70, s[12:13], v1, v1, v68
	v_rcp_f32_e32 v71, v70
	v_div_scale_f32 v72, vcc, v68, v1, v68
	s_cmpk_gt_i32 s60, 0xff
	v_fma_f32 v73, -v70, v71, 1.0
	v_fmac_f32_e32 v71, v73, v71
	v_mul_f32_e32 v73, v72, v71
	v_fma_f32 v74, -v70, v73, v72
	v_fmac_f32_e32 v73, v74, v71
	v_fma_f32 v70, -v70, v73, v72
	v_div_fmas_f32 v70, v70, v71, v73
	v_div_fixup_f32 v68, v70, v1, v68
	s_mov_b64 s[12:13], -1
	s_cbranch_scc0 .LBB0_940
	v_lshl_add_u64 v[70:71], s[60:61], 2, v[148:149]
	global_store_dword v[70:71], v68, off offset:-1024
	s_mov_b64 s[12:13], 0

; __device__ __forceinline__ void router_tail(const Ctx& F, const float (&lg)[16], const int b, const int t, const bool valid) {
;     const bool b5 = (F.lane & 32) != 0, b4 = (F.lane & 16) != 0, b3 = (F.lane & 8) != 0, b2 = (F.lane & 4) != 0;
;     float r8[8], r4[4], r2[2];
; #pragma unroll
;     for (int e = 0; e < 8; ++e) { const float keep = b5 ? lg[e + 8] : lg[e], send = b5 ? lg[e] : lg[e + 8]; r8[e] = keep + __shfl_xor(send, 32); }
; #pragma unroll
;     for (int e = 0; e < 4; ++e) { const float keep = b4 ? r8[e + 4] : r8[e], send = b4 ? r8[e] : r8[e + 4]; r4[e] = keep + __shfl_xor(send, 16); }
; #pragma unroll
;     for (int e = 0; e < 2; ++e) { const float keep = b3 ? r4[e + 2] : r4[e], send = b3 ? r4[e] : r4[e + 2]; r2[e] = keep + __shfl_xor(send, 8); }
;     float lgt; { const float keep = b2 ? r2[1] : r2[0], send = b2 ? r2[0] : r2[1]; lgt = keep + __shfl_xor(send, 4); }
;     lgt += __shfl_xor(lgt, 2); lgt += __shfl_xor(lgt, 1);
;     float mx = lgt;
;     mx = fmaxf(mx, __shfl_xor(mx, 4)); mx = fmaxf(mx, __shfl_xor(mx, 8)); mx = fmaxf(mx, __shfl_xor(mx, 16)); mx = fmaxf(mx, __shfl_xor(mx, 32));
;     const float ex = expf(lgt - mx); float sum = ex;
;     sum += __shfl_xor(sum, 4); sum += __shfl_xor(sum, 8); sum += __shfl_xor(sum, 16); sum += __shfl_xor(sum, 32);
;     if (valid && (F.lane & 3) == 0) { const float af = ex / sum; const int e = F.lane >> 2;
;         if (t < CTXL) F.affc[((size_t)(b * 16 + e)) * CTXL + t] = af; else F.affl[((size_t)(b * 16 + e)) * SEQ + (t - CTXL)] = af; }
; }
.LBB0_942:
	s_or_b64 exec, exec, s[0:1]
	s_and_b64 s[8:9], s[6:7], s[8:9]
	s_waitcnt lgkmcnt(0)
	s_nop 1
	v_permlane32_swap_b32_e32 v153, v169
	v_permlane32_swap_b32_e32 v155, v171
	v_permlane32_swap_b32_e32 v157, v173
	v_permlane32_swap_b32_e32 v159, v175
	v_permlane32_swap_b32_e32 v161, v177
	v_permlane32_swap_b32_e32 v163, v179
	v_permlane32_swap_b32_e32 v165, v181
	v_permlane32_swap_b32_e32 v167, v69
	v_add_f32_e32 v1, v153, v169
	v_add_f32_e32 v68, v155, v171
	v_add_f32_e32 v70, v157, v173
	v_add_f32_e32 v71, v159, v175
	v_add_f32_e32 v72, v161, v177
	v_add_f32_e32 v73, v163, v179
	v_add_f32_e32 v74, v165, v181
	v_add_f32_e32 v69, v167, v69
	s_waitcnt lgkmcnt(0)
	v_cndmask_b32_e64 v75, v72, v1, s[40:41]
	v_cndmask_b32_e64 v1, v1, v72, s[40:41]
	v_cndmask_b32_e64 v72, v73, v68, s[40:41]
	v_cndmask_b32_e64 v68, v68, v73, s[40:41]
	ds_bpermute_b32 v68, v193, v68
	ds_bpermute_b32 v1, v193, v1
	s_waitcnt lgkmcnt(1)
	v_add_f32_e32 v68, v72, v68
	v_cndmask_b32_e64 v72, v74, v70, s[40:41]
	v_cndmask_b32_e64 v70, v70, v74, s[40:41]
	ds_bpermute_b32 v70, v193, v70
	s_waitcnt lgkmcnt(1)
	v_add_f32_e32 v1, v75, v1
	s_waitcnt lgkmcnt(0)
	v_add_f32_e32 v70, v72, v70
	v_cndmask_b32_e64 v72, v69, v71, s[40:41]
	v_cndmask_b32_e64 v69, v71, v69, s[40:41]
	ds_bpermute_b32 v69, v193, v69
	v_cndmask_b32_e64 v71, v70, v1, s[42:43]
	v_cndmask_b32_e64 v1, v1, v70, s[42:43]
	ds_bpermute_b32 v1, v192, v1
	s_waitcnt lgkmcnt(1)
	v_add_f32_e32 v69, v72, v69
	v_cndmask_b32_e64 v70, v69, v68, s[42:43]
	v_cndmask_b32_e64 v68, v68, v69, s[42:43]
	ds_bpermute_b32 v68, v192, v68
	s_waitcnt lgkmcnt(1)
	v_add_f32_e32 v1, v71, v1
	s_waitcnt lgkmcnt(0)
	v_add_f32_e32 v68, v70, v68
	v_cndmask_b32_e64 v69, v68, v1, s[4:5]
	v_cndmask_b32_e64 v1, v1, v68, s[4:5]
	ds_bpermute_b32 v1, v191, v1
	s_waitcnt lgkmcnt(0)
	v_add_f32_e32 v1, v69, v1
	s_nop 1
	v_add_f32_dpp v1, v1, v1 quad_perm:[2,3,0,1] row_mask:0xf bank_mask:0xf
	s_nop 1
	v_add_f32_dpp v1, v1, v1 quad_perm:[1,0,3,2] row_mask:0xf bank_mask:0xf
	s_nop 1
	v_max_f32_dpp v68, v1, v1 row_half_mirror row_mask:0xf bank_mask:0xf
	s_nop 1
	v_max_f32_dpp v68, v68, v68 row_mirror row_mask:0xf bank_mask:0xf
	v_mov_b32_e32 v69, v68
	s_nop 1
	v_permlane16_swap_b32_e32 v68, v69
	v_max_f32_e32 v68, v68, v69
	v_mov_b32_e32 v69, v68
	s_nop 1
	v_permlane32_swap_b32_e32 v68, v69
	v_max_f32_e32 v68, v68, v69
	v_sub_f32_e32 v1, v1, v68
	v_mul_f32_e32 v68, 0x3fb8aa3b, v1
	v_fma_f32 v69, v1, s55, -v68
	v_rndne_f32_e32 v70, v68
	v_fmac_f32_e32 v69, 0x32a5705f, v1
	v_sub_f32_e32 v68, v68, v70
	v_add_f32_e32 v68, v68, v69
	v_exp_f32_e32 v68, v68
	v_cvt_i32_f32_e32 v69, v70
	v_cmp_ngt_f32_e32 vcc, s56, v1
	v_ldexp_f32 v68, v68, v69
	s_nop 0
	v_cndmask_b32_e32 v68, 0, v68, vcc
	v_cmp_nlt_f32_e32 vcc, s57, v1
	s_nop 1
	v_cndmask_b32_e32 v68, v222, v68, vcc
	s_nop 1
	v_add_f32_dpp v1, v68, v68 row_half_mirror row_mask:0xf bank_mask:0xf
	s_nop 1
	v_add_f32_dpp v1, v1, v1 row_mirror row_mask:0xf bank_mask:0xf
	v_mov_b32_e32 v69, v1
	s_nop 1
	v_permlane16_swap_b32_e32 v1, v69
	v_add_f32_e32 v69, v1, v69
	ds_bpermute_b32 v70, v194, v69
	s_and_saveexec_b64 s[0:1], s[8:9]
	s_cbranch_execz .LBB0_911
	s_waitcnt lgkmcnt(0)
	v_add_f32_e32 v1, v69, v70
	v_div_scale_f32 v69, s[8:9], v1, v1, v68
	v_rcp_f32_e32 v70, v69
	v_div_scale_f32 v71, vcc, v68, v1, v68
	s_cmpk_gt_i32 s2, 0xff
	v_fma_f32 v72, -v69, v70, 1.0
	v_fmac_f32_e32 v70, v72, v70
	v_mul_f32_e32 v72, v71, v70
	v_fma_f32 v73, -v69, v72, v71
	v_fmac_f32_e32 v72, v73, v70
	v_fma_f32 v69, -v69, v72, v71
	v_div_fmas_f32 v69, v69, v70, v72
	v_div_fixup_f32 v68, v69, v1, v68
	s_mov_b64 s[8:9], -1
	s_cbranch_scc0 .LBB0_945
	s_mov_b32 s3, s61
	v_lshl_add_u64 v[70:71], s[2:3], 2, v[148:149]
	global_store_dword v[70:71], v68, off offset:-1024
	s_mov_b64 s[8:9], 0
